# int8 SwiGLU units: accumulator zeroing replaced by peeled first K iteration with SrcC=0; leading half's align barrier moved behind the epilogue's conversion block
# speedup vs baseline: 1.0098x; 1.0098x over previous
.LBB0_488:
	s_add_u32 s6, s66, 0x51a00000
	s_addc_u32 s7, s67, 0
	s_lshl_b32 s8, s89, 5
	s_and_b32 s40, s8, 0x60
	s_lshl_b32 s39, s1, 6
	s_lshl_b32 s1, s1, 13
	s_lshr_b32 s12, s40, 3
	s_cmpk_lt_u32 s94, 0x100
	s_cselect_b64 s[8:9], -1, 0
	s_ashr_i32 s41, s87, 31
	s_lshl_b32 s10, s40, 2
	s_add_u32 s10, s66, s10
	s_addc_u32 s11, s67, 0
	s_add_u32 s42, s10, 0x508000
	s_addc_u32 s43, s11, 0
	s_mov_b64 s[10:11], 0x80
	v_lshl_add_u64 v[6:7], v[6:7], 0, s[10:11]
	s_add_i32 m0, s23, 0x18000
	s_waitcnt vmcnt(2)
	s_barrier
	global_load_lds_dwordx4 v[6:7], off
	v_lshl_add_u64 v[4:5], v[4:5], 0, s[10:11]
	s_add_i32 m0, s23, 0x1a000
	s_add_i32 s44, s23, 0x8000
	s_add_i32 s45, s23, 0xa000
	global_load_lds_dwordx4 v[4:5], off
	v_lshl_add_u64 v[2:3], v[2:3], 0, s[10:11]
	s_mov_b32 m0, s44
	s_add_u32 s14, s26, 0x40080
	global_load_lds_dwordx4 v[2:3], off
	v_lshl_add_u64 v[0:1], v[0:1], 0, s[10:11]
	s_mov_b32 m0, s45
	s_addc_u32 s15, s27, 0
	global_load_lds_dwordx4 v[0:1], off
	v_lshl_add_u64 v[0:1], s[14:15], 0, v[148:149]
	s_add_i32 m0, s23, 0x1c000
	s_sext_i32_i16 s49, s0
	global_load_lds_dwordx4 v[0:1], off
	v_lshl_add_u64 v[0:1], s[14:15], 0, v[144:145]
	s_add_i32 m0, s23, 0x1e000
	v_lshlrev_b32_e32 v3, 6, v8
	global_load_lds_dwordx4 v[0:1], off
	v_and_b32_e32 v1, 48, v8
	s_movk_i32 s0, 0x3c0
	v_ashrrev_i32_e32 v0, 6, v8
	v_and_or_b32 v1, v3, s0, v1
	v_lshlrev_b32_e32 v3, 2, v8
	v_lshl_add_u32 v2, v0, 10, s1
	v_and_b32_e32 v3, 32, v3
	v_add_lshl_u32 v0, v0, s12, 10
	v_bitop3_b32 v164, v1, v0, v3 bitop3:0xde
	v_lshlrev_b32_e32 v0, 14, v12
	v_and_b32_e32 v0, 0xffff8000, v0
	v_bitop3_b32 v2, v1, v2, v3 bitop3:0xde
	v_lshl_add_u32 v0, v13, 11, v0
	v_and_b32_e32 v1, 1, v12
	v_lshl_or_b32 v0, v1, 6, v0
	v_lshl_add_u32 v152, v14, 1, v0
	v_lshlrev_b32_e32 v0, 14, v9
	v_and_b32_e32 v0, 0xffff8000, v0
	s_waitcnt vmcnt(6)
	v_lshl_add_u32 v0, v10, 11, v0
	v_and_b32_e32 v1, 1, v9
	v_lshl_or_b32 v0, v1, 6, v0
	s_add_i32 s46, 0, 0x10000
	s_add_i32 s47, 0, 0x14000
	v_mov_b32_e32 v153, v149
	v_lshl_add_u32 v154, v11, 1, v0
	v_mov_b32_e32 v155, v149
	v_mov_b64_e32 v[156:157], 0xb00
	v_mov_b64_e32 v[158:159], 0xaff
	v_add_u32_e32 v165, s46, v164
	v_add_u32_e32 v166, s47, v164
	v_add_u32_e32 v167, 0, v2
	s_mov_b32 s12, 0xbfb8aa3b
	s_movk_i32 s48, 0x1600
	s_mov_b64 s[20:21], s[26:27]
	s_mov_b64 s[18:19], s[24:25]
	s_barrier
	s_waitcnt vmcnt(0)
	s_branch .LBB0_491

.LBB0_493:
	s_add_u32 s24, s24, 0x40080
	s_addc_u32 s25, s25, 0
	s_add_u32 s15, s26, 0x100
	s_addc_u32 s17, s27, 0
	s_mov_b32 s50, -2
	ds_read_b128 v[76:79], v165
	ds_read_b128 v[80:83], v165 offset:1024
	ds_read_b128 v[84:87], v165 offset:2048
	ds_read_b128 v[88:91], v165 offset:3072
	ds_read_b128 v[160:163], v166
	ds_read_b128 v[168:171], v166 offset:1024
	ds_read_b128 v[172:175], v166 offset:2048
	ds_read_b128 v[176:179], v166 offset:3072
	s_add_u32 s26, s24, 0xfffc0080
	s_addc_u32 s27, s25, -1
	s_cmp_eq_u32 s50, 12
	s_cselect_b32 s29, s19, s27
	s_cselect_b32 s28, s18, s26
	s_cselect_b32 s27, s21, s17
	s_cselect_b32 s26, s20, s15
	v_lshl_add_u64 v[212:213], s[24:25], 0, v[152:153]
	s_add_i32 m0, s23, 0xc000
	ds_read_b128 v[180:183], v167
	ds_read_b128 v[184:187], v167 offset:1024
	ds_read_b128 v[188:191], v167 offset:2048
	ds_read_b128 v[192:195], v167 offset:3072
	ds_read_b128 v[196:199], v167 offset:4096
	ds_read_b128 v[200:203], v167 offset:5120
	ds_read_b128 v[204:207], v167 offset:6144
	ds_read_b128 v[208:211], v167 offset:7168
	global_load_lds_dwordx4 v[212:213], off
	v_lshl_add_u64 v[212:213], s[24:25], 0, v[154:155]
	s_add_i32 m0, s23, 0xe000
	s_nop 0
	global_load_lds_dwordx4 v[212:213], off
	s_waitcnt vmcnt(8)
	s_waitcnt lgkmcnt(0)
	s_barrier
	s_setprio 1
	s_waitcnt lgkmcnt(0)
	v_mfma_i32_16x16x64_i8 v[140:143], v[76:79], v[180:183], 0
	v_mfma_i32_16x16x64_i8 v[136:139], v[84:87], v[180:183], 0
	v_mfma_i32_16x16x64_i8 v[124:127], v[76:79], v[188:191], 0
	v_mfma_i32_16x16x64_i8 v[120:123], v[84:87], v[188:191], 0
	v_mfma_i32_16x16x64_i8 v[108:111], v[76:79], v[196:199], 0
	v_mfma_i32_16x16x64_i8 v[104:107], v[84:87], v[196:199], 0
	v_mfma_i32_16x16x64_i8 v[92:95], v[76:79], v[204:207], 0
	v_mfma_i32_16x16x64_i8 v[72:75], v[84:87], v[204:207], 0
	v_mfma_i32_16x16x64_i8 v[140:143], v[80:83], v[184:187], v[140:143]
	v_mfma_i32_16x16x64_i8 v[136:139], v[88:91], v[184:187], v[136:139]
	v_mfma_i32_16x16x64_i8 v[124:127], v[80:83], v[192:195], v[124:127]
	v_mfma_i32_16x16x64_i8 v[120:123], v[88:91], v[192:195], v[120:123]
	v_mfma_i32_16x16x64_i8 v[108:111], v[80:83], v[200:203], v[108:111]
	v_mfma_i32_16x16x64_i8 v[104:107], v[88:91], v[200:203], v[104:107]
	v_mfma_i32_16x16x64_i8 v[92:95], v[80:83], v[208:211], v[92:95]
	v_mfma_i32_16x16x64_i8 v[72:75], v[88:91], v[208:211], v[72:75]
	s_setprio 0
	s_setprio 1
	v_mfma_i32_16x16x64_i8 v[132:135], v[160:163], v[180:183], 0
	v_mfma_i32_16x16x64_i8 v[128:131], v[172:175], v[180:183], 0
	v_mfma_i32_16x16x64_i8 v[116:119], v[160:163], v[188:191], 0
	v_mfma_i32_16x16x64_i8 v[112:115], v[172:175], v[188:191], 0
	v_mfma_i32_16x16x64_i8 v[100:103], v[160:163], v[196:199], 0
	v_mfma_i32_16x16x64_i8 v[96:99], v[172:175], v[196:199], 0
	v_mfma_i32_16x16x64_i8 v[68:71], v[160:163], v[204:207], 0
	v_mfma_i32_16x16x64_i8 v[64:67], v[172:175], v[204:207], 0
	v_mfma_i32_16x16x64_i8 v[132:135], v[168:171], v[184:187], v[132:135]
	v_mfma_i32_16x16x64_i8 v[128:131], v[176:179], v[184:187], v[128:131]
	v_mfma_i32_16x16x64_i8 v[116:119], v[168:171], v[192:195], v[116:119]
	v_mfma_i32_16x16x64_i8 v[112:115], v[176:179], v[192:195], v[112:115]
	v_mfma_i32_16x16x64_i8 v[100:103], v[168:171], v[200:203], v[100:103]
	v_mfma_i32_16x16x64_i8 v[96:99], v[176:179], v[200:203], v[96:99]
	v_mfma_i32_16x16x64_i8 v[68:71], v[168:171], v[208:211], v[68:71]
	v_mfma_i32_16x16x64_i8 v[64:67], v[176:179], v[208:211], v[64:67]
	s_setprio 0
	s_barrier
	s_add_i32 s51, s46, s31
	v_lshl_add_u64 v[212:213], s[26:27], 0, v[148:149]
	s_mov_b32 m0, s51
	ds_read_b128 v[180:183], v167 offset:16384
	ds_read_b128 v[184:187], v167 offset:17408
	ds_read_b128 v[188:191], v167 offset:18432
	ds_read_b128 v[192:195], v167 offset:19456
	ds_read_b128 v[196:199], v167 offset:20480
	ds_read_b128 v[200:203], v167 offset:21504
	ds_read_b128 v[204:207], v167 offset:22528
	ds_read_b128 v[208:211], v167 offset:23552
	global_load_lds_dwordx4 v[212:213], off
	s_add_i32 m0, s51, 0x2000
	s_add_u32 s52, s26, 0x40000
	v_lshl_add_u64 v[214:215], s[26:27], 0, v[144:145]
	s_addc_u32 s53, s27, 0
	s_add_i32 s51, s47, s31
	global_load_lds_dwordx4 v[214:215], off
	v_lshl_add_u64 v[216:217], s[52:53], 0, v[148:149]
	s_mov_b32 m0, s51
	v_lshl_add_u64 v[218:219], s[28:29], 0, v[146:147]
	global_load_lds_dwordx4 v[216:217], off
	v_lshl_add_u64 v[216:217], s[52:53], 0, v[144:145]
	s_add_i32 m0, s51, 0x2000
	s_nop 0
	global_load_lds_dwordx4 v[216:217], off
	v_lshl_add_u64 v[216:217], s[28:29], 0, v[150:151]
	s_mov_b32 m0, s23
	s_nop 0
	global_load_lds_dwordx4 v[216:217], off
	s_mov_b32 m0, s35
	s_nop 0
	global_load_lds_dwordx4 v[218:219], off
	s_waitcnt vmcnt(8)
	s_waitcnt lgkmcnt(0)
	s_barrier
	s_setprio 1
	s_waitcnt lgkmcnt(0)
	v_mfma_i32_16x16x64_i8 v[60:63], v[76:79], v[180:183], 0
	v_mfma_i32_16x16x64_i8 v[56:59], v[84:87], v[180:183], 0
	v_mfma_i32_16x16x64_i8 v[44:47], v[76:79], v[188:191], 0
	v_mfma_i32_16x16x64_i8 v[40:43], v[84:87], v[188:191], 0
	v_mfma_i32_16x16x64_i8 v[28:31], v[76:79], v[196:199], 0
	v_mfma_i32_16x16x64_i8 v[24:27], v[84:87], v[196:199], 0
	v_mfma_i32_16x16x64_i8 v[12:15], v[76:79], v[204:207], 0
	v_mfma_i32_16x16x64_i8 v[8:11], v[84:87], v[204:207], 0
	v_mfma_i32_16x16x64_i8 v[60:63], v[80:83], v[184:187], v[60:63]
	v_mfma_i32_16x16x64_i8 v[56:59], v[88:91], v[184:187], v[56:59]
	v_mfma_i32_16x16x64_i8 v[44:47], v[80:83], v[192:195], v[44:47]
	v_mfma_i32_16x16x64_i8 v[40:43], v[88:91], v[192:195], v[40:43]
	v_mfma_i32_16x16x64_i8 v[28:31], v[80:83], v[200:203], v[28:31]
	v_mfma_i32_16x16x64_i8 v[24:27], v[88:91], v[200:203], v[24:27]
	v_mfma_i32_16x16x64_i8 v[12:15], v[80:83], v[208:211], v[12:15]
	v_mfma_i32_16x16x64_i8 v[8:11], v[88:91], v[208:211], v[8:11]
	s_setprio 0
	s_setprio 1
	v_mfma_i32_16x16x64_i8 v[52:55], v[160:163], v[180:183], 0
	v_mfma_i32_16x16x64_i8 v[48:51], v[172:175], v[180:183], 0
	v_mfma_i32_16x16x64_i8 v[36:39], v[160:163], v[188:191], 0
	v_mfma_i32_16x16x64_i8 v[32:35], v[172:175], v[188:191], 0
	v_mfma_i32_16x16x64_i8 v[20:23], v[160:163], v[196:199], 0
	v_mfma_i32_16x16x64_i8 v[16:19], v[172:175], v[196:199], 0
	v_mfma_i32_16x16x64_i8 v[4:7], v[160:163], v[204:207], 0
	v_mfma_i32_16x16x64_i8 v[0:3], v[172:175], v[204:207], 0
	v_mfma_i32_16x16x64_i8 v[52:55], v[168:171], v[184:187], v[52:55]
	v_mfma_i32_16x16x64_i8 v[48:51], v[176:179], v[184:187], v[48:51]
	v_mfma_i32_16x16x64_i8 v[36:39], v[168:171], v[192:195], v[36:39]
	v_mfma_i32_16x16x64_i8 v[32:35], v[176:179], v[192:195], v[32:35]
	v_mfma_i32_16x16x64_i8 v[20:23], v[168:171], v[200:203], v[20:23]
	v_mfma_i32_16x16x64_i8 v[16:19], v[176:179], v[200:203], v[16:19]
	v_mfma_i32_16x16x64_i8 v[4:7], v[168:171], v[208:211], v[4:7]
	v_mfma_i32_16x16x64_i8 v[0:3], v[176:179], v[208:211], v[0:3]
	s_setprio 0
	s_barrier
	s_add_i32 s51, 0, 0x18000
	s_add_i32 s52, 0, 0x1c000
	v_add_u32_e32 v88, s51, v164
	v_add_u32_e32 v176, s52, v164
	ds_read_b128 v[76:79], v88
	ds_read_b128 v[80:83], v88 offset:1024
	ds_read_b128 v[84:87], v88 offset:2048
	ds_read_b128 v[88:91], v88 offset:3072
	ds_read_b128 v[160:163], v176
	ds_read_b128 v[168:171], v176 offset:1024
	ds_read_b128 v[172:175], v176 offset:2048
	ds_read_b128 v[176:179], v176 offset:3072
	s_add_u32 s28, s28, 0x40000
	s_addc_u32 s29, s29, 0
	s_mov_b32 m0, s36
	v_lshl_add_u64 v[220:221], s[28:29], 0, v[150:151]
	ds_read_b128 v[180:183], v167 offset:32768
	ds_read_b128 v[184:187], v167 offset:33792
	ds_read_b128 v[188:191], v167 offset:34816
	ds_read_b128 v[192:195], v167 offset:35840
	ds_read_b128 v[196:199], v167 offset:36864
	ds_read_b128 v[200:203], v167 offset:37888
	ds_read_b128 v[204:207], v167 offset:38912
	ds_read_b128 v[208:211], v167 offset:39936
	global_load_lds_dwordx4 v[220:221], off
	v_lshl_add_u64 v[220:221], s[28:29], 0, v[146:147]
	s_mov_b32 m0, s37
	s_nop 0
	global_load_lds_dwordx4 v[220:221], off
	s_waitcnt vmcnt(8)
	s_waitcnt lgkmcnt(0)
	s_barrier
	s_setprio 1
	s_waitcnt lgkmcnt(0)
	v_mfma_i32_16x16x64_i8 v[140:143], v[76:79], v[180:183], v[140:143]
	v_mfma_i32_16x16x64_i8 v[136:139], v[84:87], v[180:183], v[136:139]
	v_mfma_i32_16x16x64_i8 v[124:127], v[76:79], v[188:191], v[124:127]
	v_mfma_i32_16x16x64_i8 v[120:123], v[84:87], v[188:191], v[120:123]
	v_mfma_i32_16x16x64_i8 v[108:111], v[76:79], v[196:199], v[108:111]
	v_mfma_i32_16x16x64_i8 v[104:107], v[84:87], v[196:199], v[104:107]
	v_mfma_i32_16x16x64_i8 v[92:95], v[76:79], v[204:207], v[92:95]
	v_mfma_i32_16x16x64_i8 v[72:75], v[84:87], v[204:207], v[72:75]
	v_mfma_i32_16x16x64_i8 v[140:143], v[80:83], v[184:187], v[140:143]
	v_mfma_i32_16x16x64_i8 v[136:139], v[88:91], v[184:187], v[136:139]
	v_mfma_i32_16x16x64_i8 v[124:127], v[80:83], v[192:195], v[124:127]
	v_mfma_i32_16x16x64_i8 v[120:123], v[88:91], v[192:195], v[120:123]
	v_mfma_i32_16x16x64_i8 v[108:111], v[80:83], v[200:203], v[108:111]
	v_mfma_i32_16x16x64_i8 v[104:107], v[88:91], v[200:203], v[104:107]
	v_mfma_i32_16x16x64_i8 v[92:95], v[80:83], v[208:211], v[92:95]
	v_mfma_i32_16x16x64_i8 v[72:75], v[88:91], v[208:211], v[72:75]
	s_setprio 0
	s_setprio 1
	v_mfma_i32_16x16x64_i8 v[132:135], v[160:163], v[180:183], v[132:135]
	v_mfma_i32_16x16x64_i8 v[128:131], v[172:175], v[180:183], v[128:131]
	v_mfma_i32_16x16x64_i8 v[116:119], v[160:163], v[188:191], v[116:119]
	v_mfma_i32_16x16x64_i8 v[112:115], v[172:175], v[188:191], v[112:115]
	v_mfma_i32_16x16x64_i8 v[100:103], v[160:163], v[196:199], v[100:103]
	v_mfma_i32_16x16x64_i8 v[96:99], v[172:175], v[196:199], v[96:99]
	v_mfma_i32_16x16x64_i8 v[68:71], v[160:163], v[204:207], v[68:71]
	v_mfma_i32_16x16x64_i8 v[64:67], v[172:175], v[204:207], v[64:67]
	v_mfma_i32_16x16x64_i8 v[132:135], v[168:171], v[184:187], v[132:135]
	v_mfma_i32_16x16x64_i8 v[128:131], v[176:179], v[184:187], v[128:131]
	v_mfma_i32_16x16x64_i8 v[116:119], v[168:171], v[192:195], v[116:119]
	v_mfma_i32_16x16x64_i8 v[112:115], v[176:179], v[192:195], v[112:115]
	v_mfma_i32_16x16x64_i8 v[100:103], v[168:171], v[200:203], v[100:103]
	v_mfma_i32_16x16x64_i8 v[96:99], v[176:179], v[200:203], v[96:99]
	v_mfma_i32_16x16x64_i8 v[68:71], v[168:171], v[208:211], v[68:71]
	v_mfma_i32_16x16x64_i8 v[64:67], v[176:179], v[208:211], v[64:67]
	s_setprio 0
	s_barrier
	s_add_i32 s28, s51, s31
	v_lshl_add_u64 v[212:213], v[212:213], 0, s[10:11]
	s_mov_b32 m0, s28
	ds_read_b128 v[180:183], v167 offset:49152
	ds_read_b128 v[184:187], v167 offset:50176
	ds_read_b128 v[188:191], v167 offset:51200
	ds_read_b128 v[192:195], v167 offset:52224
	ds_read_b128 v[196:199], v167 offset:53248
	ds_read_b128 v[200:203], v167 offset:54272
	ds_read_b128 v[204:207], v167 offset:55296
	ds_read_b128 v[208:211], v167 offset:56320
	global_load_lds_dwordx4 v[212:213], off
	s_add_i32 m0, s28, 0x2000
	s_add_u32 s26, s26, 0x40080
	v_lshl_add_u64 v[212:213], v[214:215], 0, s[10:11]
	s_addc_u32 s27, s27, 0
	s_add_i32 s28, s52, s31
	global_load_lds_dwordx4 v[212:213], off
	v_lshl_add_u64 v[212:213], s[26:27], 0, v[148:149]
	s_mov_b32 m0, s28
	s_nop 0
	global_load_lds_dwordx4 v[212:213], off
	v_lshl_add_u64 v[212:213], s[26:27], 0, v[144:145]
	s_add_i32 m0, s28, 0x2000
	s_nop 0
	global_load_lds_dwordx4 v[212:213], off
	v_lshl_add_u64 v[212:213], v[216:217], 0, s[10:11]
	s_mov_b32 m0, s44
	s_nop 0
	global_load_lds_dwordx4 v[212:213], off
	v_lshl_add_u64 v[212:213], v[218:219], 0, s[10:11]
	s_mov_b32 m0, s45
	s_nop 0
	global_load_lds_dwordx4 v[212:213], off
	s_waitcnt vmcnt(8)
	s_waitcnt lgkmcnt(0)
	s_barrier
	s_setprio 1
	s_waitcnt lgkmcnt(0)
	v_mfma_i32_16x16x64_i8 v[60:63], v[76:79], v[180:183], v[60:63]
	v_mfma_i32_16x16x64_i8 v[56:59], v[84:87], v[180:183], v[56:59]
	v_mfma_i32_16x16x64_i8 v[44:47], v[76:79], v[188:191], v[44:47]
	v_mfma_i32_16x16x64_i8 v[40:43], v[84:87], v[188:191], v[40:43]
	v_mfma_i32_16x16x64_i8 v[28:31], v[76:79], v[196:199], v[28:31]
	v_mfma_i32_16x16x64_i8 v[24:27], v[84:87], v[196:199], v[24:27]
	v_mfma_i32_16x16x64_i8 v[12:15], v[76:79], v[204:207], v[12:15]
	v_mfma_i32_16x16x64_i8 v[8:11], v[84:87], v[204:207], v[8:11]
	v_mfma_i32_16x16x64_i8 v[60:63], v[80:83], v[184:187], v[60:63]
	v_mfma_i32_16x16x64_i8 v[56:59], v[88:91], v[184:187], v[56:59]
	v_mfma_i32_16x16x64_i8 v[44:47], v[80:83], v[192:195], v[44:47]
	v_mfma_i32_16x16x64_i8 v[40:43], v[88:91], v[192:195], v[40:43]
	v_mfma_i32_16x16x64_i8 v[28:31], v[80:83], v[200:203], v[28:31]
	v_mfma_i32_16x16x64_i8 v[24:27], v[88:91], v[200:203], v[24:27]
	v_mfma_i32_16x16x64_i8 v[12:15], v[80:83], v[208:211], v[12:15]
	v_mfma_i32_16x16x64_i8 v[8:11], v[88:91], v[208:211], v[8:11]
	s_setprio 0
	s_setprio 1
	v_mfma_i32_16x16x64_i8 v[52:55], v[160:163], v[180:183], v[52:55]
	v_mfma_i32_16x16x64_i8 v[48:51], v[172:175], v[180:183], v[48:51]
	v_mfma_i32_16x16x64_i8 v[36:39], v[160:163], v[188:191], v[36:39]
	v_mfma_i32_16x16x64_i8 v[32:35], v[172:175], v[188:191], v[32:35]
	v_mfma_i32_16x16x64_i8 v[20:23], v[160:163], v[196:199], v[20:23]
	v_mfma_i32_16x16x64_i8 v[16:19], v[172:175], v[196:199], v[16:19]
	v_mfma_i32_16x16x64_i8 v[4:7], v[160:163], v[204:207], v[4:7]
	v_mfma_i32_16x16x64_i8 v[0:3], v[172:175], v[204:207], v[0:3]
	v_mfma_i32_16x16x64_i8 v[52:55], v[168:171], v[184:187], v[52:55]
	v_mfma_i32_16x16x64_i8 v[48:51], v[176:179], v[184:187], v[48:51]
	v_mfma_i32_16x16x64_i8 v[36:39], v[168:171], v[192:195], v[36:39]
	v_mfma_i32_16x16x64_i8 v[32:35], v[176:179], v[192:195], v[32:35]
	v_mfma_i32_16x16x64_i8 v[20:23], v[168:171], v[200:203], v[20:23]
	v_mfma_i32_16x16x64_i8 v[16:19], v[176:179], v[200:203], v[16:19]
	v_mfma_i32_16x16x64_i8 v[4:7], v[168:171], v[208:211], v[4:7]
	v_mfma_i32_16x16x64_i8 v[0:3], v[176:179], v[208:211], v[0:3]
	s_setprio 0
	s_barrier
	s_add_i32 s50, s50, 2
	s_add_u32 s24, s24, 0x100
	s_addc_u32 s25, s25, 0
	s_add_u32 s15, s15, 0x100
	s_addc_u32 s17, s17, 0

.LBB0_497:
	s_lshl_b32 s24, s49, 8
	v_mbcnt_lo_u32_b32 v78, -1, 0
	v_mbcnt_hi_u32_b32 v78, -1, v78
	s_lshl_b32 s15, s49, 7
	s_ashr_i32 s25, s24, 31
	v_ashrrev_i32_e32 v76, 1, v78
	s_or_b32 s15, s15, s40
	s_lshl_b64 s[24:25], s[24:25], 2
	v_and_or_b32 v78, v78, 15, s39
	v_and_b32_e32 v168, -8, v76
	s_add_u32 s24, s42, s24
	v_lshl_add_u32 v160, s22, 8, v78
	s_addc_u32 s25, s43, s25
	v_ashrrev_i32_e32 v169, 31, v168
	v_ashrrev_i32_e32 v161, 31, v160
	v_lshl_add_u64 v[76:77], v[168:169], 2, s[24:25]
	v_lshl_add_u64 v[162:163], v[160:161], 2, s[82:83]
	global_load_dword v170, v[162:163], off
	global_load_dwordx4 v[88:91], v[76:77], off
	global_load_dwordx4 v[84:87], v[76:77], off offset:16
	global_load_dwordx4 v[80:83], v[76:77], off offset:512
	s_nop 0
	global_load_dwordx4 v[76:79], v[76:77], off offset:528
	global_load_dword v196, v[162:163], off offset:64
	global_load_dword v198, v[162:163], off offset:128
	global_load_dword v200, v[162:163], off offset:192
	global_load_dword v202, v[162:163], off offset:512
	global_load_dword v204, v[162:163], off offset:576
	global_load_dword v206, v[162:163], off offset:640
	global_load_dword v208, v[162:163], off offset:704
	v_cvt_f32_i32_e32 v141, v141
	v_cvt_f32_i32_e32 v140, v140
	v_cvt_f32_i32_e32 v137, v137
	v_cvt_f32_i32_e32 v136, v136
	v_cvt_f32_i32_e32 v143, v143
	v_cvt_f32_i32_e32 v142, v142
	v_cvt_f32_i32_e32 v139, v139
	v_cvt_f32_i32_e32 v138, v138
	v_cvt_f32_i32_e32 v133, v133
	v_cvt_f32_i32_e32 v132, v132
	v_cvt_f32_i32_e32 v135, v135
	v_cvt_f32_i32_e32 v134, v134
	v_cvt_f32_i32_e32 v175, v131
	v_cvt_f32_i32_e32 v174, v130
	v_cvt_f32_i32_e32 v173, v129
	v_cvt_f32_i32_e32 v172, v128
	v_mov_b32_e32 v176, 0
	v_mov_b32_e32 v177, 0
	v_mov_b64_e32 v[130:131], s[6:7]
	v_add_u32_e32 v128, s15, v168
	v_mad_i64_i32 v[168:169], s[24:25], v160, s48, v[130:131]
	v_or_b32_e32 v178, 16, v160
	v_ashrrev_i32_e32 v129, 31, v128
	v_ashrrev_i32_e32 v179, 31, v178
	v_cvt_f32_i32_e32 v125, v125
	v_cvt_f32_i32_e32 v124, v124
	v_cvt_f32_i32_e32 v121, v121
	v_cvt_f32_i32_e32 v120, v120
	v_cvt_f32_i32_e32 v127, v127
	v_cvt_f32_i32_e32 v126, v126
	v_cvt_f32_i32_e32 v123, v123
	v_cvt_f32_i32_e32 v122, v122
	v_cvt_f32_i32_e32 v113, v113
	v_cvt_f32_i32_e32 v112, v112
	v_cvt_f32_i32_e32 v115, v115
	v_cvt_f32_i32_e32 v114, v114
	v_cvt_f32_i32_e32 v117, v117
	v_cvt_f32_i32_e32 v116, v116
	v_cvt_f32_i32_e32 v119, v119
	v_cvt_f32_i32_e32 v118, v118
	v_cvt_f32_i32_e32 v109, v109
	v_cvt_f32_i32_e32 v108, v108
	v_cvt_f32_i32_e32 v105, v105
	v_cvt_f32_i32_e32 v104, v104
	v_cvt_f32_i32_e32 v111, v111
	v_cvt_f32_i32_e32 v110, v110
	v_cvt_f32_i32_e32 v107, v107
	v_cvt_f32_i32_e32 v106, v106
	v_cvt_f32_i32_e32 v97, v97
	v_cvt_f32_i32_e32 v96, v96
	v_cvt_f32_i32_e32 v99, v99
	v_cvt_f32_i32_e32 v98, v98
	v_cvt_f32_i32_e32 v101, v101
	v_cvt_f32_i32_e32 v100, v100
	v_cvt_f32_i32_e32 v103, v103
	v_cvt_f32_i32_e32 v102, v102
	v_cvt_f32_i32_e32 v93, v93
	v_cvt_f32_i32_e32 v92, v92
	v_cvt_f32_i32_e32 v73, v73
	v_cvt_f32_i32_e32 v72, v72
	v_cvt_f32_i32_e32 v95, v95
	v_cvt_f32_i32_e32 v94, v94
	v_cvt_f32_i32_e32 v75, v75
	v_cvt_f32_i32_e32 v74, v74
	v_cvt_f32_i32_e32 v65, v65
	v_cvt_f32_i32_e32 v64, v64
	v_cvt_f32_i32_e32 v67, v67
	v_cvt_f32_i32_e32 v66, v66
	v_cvt_f32_i32_e32 v69, v69
	v_cvt_f32_i32_e32 v68, v68
	v_cvt_f32_i32_e32 v71, v71
	v_cvt_f32_i32_e32 v70, v70
	v_cvt_f32_i32_e32 v61, v61
	v_cvt_f32_i32_e32 v60, v60
	v_cvt_f32_i32_e32 v57, v57
	s_and_b64 vcc, exec, s[8:9]
	s_cbranch_vccz .Lalign_p3
	s_barrier
.Lalign_p3:
	s_waitcnt vmcnt(7)
	v_pk_mul_f32 v[182:183], v[88:89], v[170:171] op_sel_hi:[1,0]
	v_pk_mul_f32 v[186:187], v[84:85], v[170:171] op_sel_hi:[1,0]
	v_pk_mul_f32 v[180:181], v[90:91], v[170:171] op_sel_hi:[1,0]
	v_pk_mul_f32 v[184:185], v[86:87], v[170:171] op_sel_hi:[1,0]
	v_pk_mul_f32 v[188:189], v[80:81], v[170:171] op_sel_hi:[1,0]
	v_pk_mul_f32 v[190:191], v[82:83], v[170:171] op_sel_hi:[1,0]
	v_pk_mul_f32 v[140:141], v[182:183], v[140:141]
	v_pk_mul_f32 v[136:137], v[186:187], v[136:137]
	v_pk_mul_f32 v[192:193], v[76:77], v[170:171] op_sel_hi:[1,0]
	v_pk_mul_f32 v[170:171], v[78:79], v[170:171] op_sel_hi:[1,0]
	v_pk_mul_f32 v[142:143], v[180:181], v[142:143]
	v_pk_mul_f32 v[138:139], v[184:185], v[138:139]
	v_pk_mul_f32 v[134:135], v[190:191], v[134:135]
	v_pk_mul_f32 v[132:133], v[188:189], v[132:133]
	v_pk_mul_f32 v[180:181], v[140:141], s[12:13] op_sel_hi:[1,0]
	v_pk_mul_f32 v[184:185], v[136:137], s[12:13] op_sel_hi:[1,0]
	v_pk_mul_f32 v[170:171], v[170:171], v[174:175]
	v_pk_mul_f32 v[174:175], v[142:143], s[12:13] op_sel_hi:[1,0]
	v_pk_mul_f32 v[132:133], v[140:141], v[132:133]
	v_pk_mul_f32 v[134:135], v[142:143], v[134:135]
	v_exp_f32_e32 v140, v180
	v_exp_f32_e32 v142, v184
	v_exp_f32_e32 v141, v181
	v_exp_f32_e32 v143, v185
	v_pk_mul_f32 v[172:173], v[192:193], v[172:173]
	v_pk_mul_f32 v[182:183], v[138:139], s[12:13] op_sel_hi:[1,0]
	v_pk_mul_f32 v[136:137], v[136:137], v[172:173]
	v_pk_mul_f32 v[138:139], v[138:139], v[170:171]
	v_exp_f32_e32 v170, v174
	v_exp_f32_e32 v171, v175
	v_exp_f32_e32 v172, v182
	v_exp_f32_e32 v173, v183
	v_pk_add_f32 v[140:141], v[140:141], 1.0 op_sel_hi:[1,0]
	v_pk_add_f32 v[142:143], v[142:143], 1.0 op_sel_hi:[1,0]
	v_rcp_f32_e32 v140, v140
	v_rcp_f32_e32 v142, v142
	v_rcp_f32_e32 v141, v141
	v_rcp_f32_e32 v143, v143
	v_pk_add_f32 v[170:171], v[170:171], 1.0 op_sel_hi:[1,0]
	v_pk_add_f32 v[172:173], v[172:173], 1.0 op_sel_hi:[1,0]
	v_rcp_f32_e32 v170, v170
	v_rcp_f32_e32 v172, v172
	v_rcp_f32_e32 v171, v171
	v_rcp_f32_e32 v173, v173
	v_pk_mul_f32 v[132:133], v[132:133], v[140:141]
	v_pk_mul_f32 v[136:137], v[136:137], v[142:143]
	v_cvt_pk_fp8_f32 v176, v132, v133
	v_cvt_pk_fp8_f32 v177, v136, v137
	v_pk_mul_f32 v[132:133], v[134:135], v[170:171]
	v_pk_mul_f32 v[134:135], v[138:139], v[172:173]
	v_cvt_pk_fp8_f32 v176, v132, v133 op_sel:[0,0,1]
	v_cvt_pk_fp8_f32 v177, v134, v135 op_sel:[0,0,1]
	v_lshl_add_u64 v[132:133], v[168:169], 0, v[128:129]
	v_or_b32_e32 v136, 32, v160
	global_store_dwordx2 v[132:133], v[176:177], off
	v_mov_b32_e32 v134, 0
	v_mov_b32_e32 v135, 0
	v_mad_i64_i32 v[138:139], s[24:25], v178, s48, v[130:131]
	v_ashrrev_i32_e32 v137, 31, v136
	v_cvt_f32_i32_e32 v56, v56
	v_cvt_f32_i32_e32 v63, v63
	v_cvt_f32_i32_e32 v62, v62
	v_cvt_f32_i32_e32 v59, v59
	v_cvt_f32_i32_e32 v58, v58
	v_cvt_f32_i32_e32 v49, v49
	v_cvt_f32_i32_e32 v48, v48
	v_cvt_f32_i32_e32 v51, v51
	v_cvt_f32_i32_e32 v50, v50
	v_cvt_f32_i32_e32 v53, v53
	v_cvt_f32_i32_e32 v52, v52
	v_cvt_f32_i32_e32 v55, v55
	v_cvt_f32_i32_e32 v54, v54
	v_cvt_f32_i32_e32 v45, v45
	v_cvt_f32_i32_e32 v44, v44
	v_cvt_f32_i32_e32 v41, v41
	v_cvt_f32_i32_e32 v40, v40
	v_cvt_f32_i32_e32 v47, v47
	v_cvt_f32_i32_e32 v46, v46
	v_cvt_f32_i32_e32 v43, v43
	v_cvt_f32_i32_e32 v42, v42
	v_cvt_f32_i32_e32 v33, v33
	v_cvt_f32_i32_e32 v32, v32
	v_cvt_f32_i32_e32 v35, v35
	v_cvt_f32_i32_e32 v34, v34
	v_cvt_f32_i32_e32 v37, v37
	v_cvt_f32_i32_e32 v36, v36
	v_cvt_f32_i32_e32 v39, v39
	v_cvt_f32_i32_e32 v38, v38
	v_cvt_f32_i32_e32 v29, v29
	v_cvt_f32_i32_e32 v28, v28
	v_cvt_f32_i32_e32 v25, v25
	v_cvt_f32_i32_e32 v24, v24
	v_cvt_f32_i32_e32 v31, v31
	v_cvt_f32_i32_e32 v30, v30
	v_cvt_f32_i32_e32 v27, v27
	v_cvt_f32_i32_e32 v26, v26
	v_cvt_f32_i32_e32 v17, v17
	v_cvt_f32_i32_e32 v16, v16
	v_cvt_f32_i32_e32 v19, v19
	v_cvt_f32_i32_e32 v18, v18
	v_cvt_f32_i32_e32 v21, v21
	v_cvt_f32_i32_e32 v20, v20
	v_cvt_f32_i32_e32 v23, v23
	v_cvt_f32_i32_e32 v22, v22
	v_cvt_f32_i32_e32 v13, v13
	v_cvt_f32_i32_e32 v12, v12
	v_cvt_f32_i32_e32 v9, v9
	v_cvt_f32_i32_e32 v8, v8
	v_cvt_f32_i32_e32 v15, v15
	v_cvt_f32_i32_e32 v14, v14
	v_cvt_f32_i32_e32 v11, v11
	v_cvt_f32_i32_e32 v10, v10
	v_cvt_f32_i32_e32 v1, v1
	v_cvt_f32_i32_e32 v0, v0
	v_cvt_f32_i32_e32 v3, v3
	v_cvt_f32_i32_e32 v2, v2
	v_cvt_f32_i32_e32 v5, v5
	v_cvt_f32_i32_e32 v4, v4
	v_cvt_f32_i32_e32 v7, v7
	v_cvt_f32_i32_e32 v6, v6
	s_andn2_b64 vcc, exec, s[0:1]
	s_mov_b64 s[0:1], -1
	s_waitcnt vmcnt(7)
	v_pk_mul_f32 v[142:143], v[88:89], v[196:197] op_sel_hi:[1,0]
	v_pk_mul_f32 v[170:171], v[84:85], v[196:197] op_sel_hi:[1,0]
	v_pk_mul_f32 v[140:141], v[90:91], v[196:197] op_sel_hi:[1,0]
	v_pk_mul_f32 v[168:169], v[86:87], v[196:197] op_sel_hi:[1,0]
	v_pk_mul_f32 v[172:173], v[80:81], v[196:197] op_sel_hi:[1,0]
	v_pk_mul_f32 v[174:175], v[82:83], v[196:197] op_sel_hi:[1,0]
	v_pk_mul_f32 v[176:177], v[76:77], v[196:197] op_sel_hi:[1,0]
	v_pk_mul_f32 v[132:133], v[78:79], v[196:197] op_sel_hi:[1,0]
	v_pk_mul_f32 v[124:125], v[142:143], v[124:125]
	v_pk_mul_f32 v[120:121], v[170:171], v[120:121]
	v_pk_mul_f32 v[126:127], v[140:141], v[126:127]
	v_pk_mul_f32 v[122:123], v[168:169], v[122:123]
	v_pk_mul_f32 v[114:115], v[132:133], v[114:115]
	v_pk_mul_f32 v[112:113], v[176:177], v[112:113]
	v_pk_mul_f32 v[140:141], v[124:125], s[12:13] op_sel_hi:[1,0]
	v_pk_mul_f32 v[168:169], v[120:121], s[12:13] op_sel_hi:[1,0]
	v_pk_mul_f32 v[142:143], v[122:123], s[12:13] op_sel_hi:[1,0]
	v_pk_mul_f32 v[112:113], v[120:121], v[112:113]
	v_pk_mul_f32 v[114:115], v[122:123], v[114:115]
	v_exp_f32_e32 v120, v140
	v_exp_f32_e32 v122, v168
	v_exp_f32_e32 v121, v141
	v_exp_f32_e32 v123, v169
	v_pk_mul_f32 v[118:119], v[174:175], v[118:119]
	v_pk_mul_f32 v[116:117], v[172:173], v[116:117]
	v_pk_mul_f32 v[132:133], v[126:127], s[12:13] op_sel_hi:[1,0]
	v_pk_mul_f32 v[116:117], v[124:125], v[116:117]
	v_pk_mul_f32 v[118:119], v[126:127], v[118:119]
	v_exp_f32_e32 v124, v132
	v_exp_f32_e32 v125, v133
	v_exp_f32_e32 v126, v142
	v_exp_f32_e32 v127, v143
	v_pk_add_f32 v[120:121], v[120:121], 1.0 op_sel_hi:[1,0]
	v_pk_add_f32 v[122:123], v[122:123], 1.0 op_sel_hi:[1,0]
	v_rcp_f32_e32 v120, v120
	v_rcp_f32_e32 v122, v122
	v_rcp_f32_e32 v121, v121
	v_rcp_f32_e32 v123, v123
	v_pk_add_f32 v[124:125], v[124:125], 1.0 op_sel_hi:[1,0]
	v_pk_add_f32 v[126:127], v[126:127], 1.0 op_sel_hi:[1,0]
	v_rcp_f32_e32 v124, v124
	v_rcp_f32_e32 v126, v126
	v_rcp_f32_e32 v125, v125
	v_rcp_f32_e32 v127, v127
	v_pk_mul_f32 v[116:117], v[116:117], v[120:121]
	v_pk_mul_f32 v[112:113], v[112:113], v[122:123]
	v_cvt_pk_fp8_f32 v134, v116, v117
	v_cvt_pk_fp8_f32 v135, v112, v113
	v_pk_mul_f32 v[112:113], v[118:119], v[124:125]
	v_pk_mul_f32 v[114:115], v[114:115], v[126:127]
	v_cvt_pk_fp8_f32 v134, v112, v113 op_sel:[0,0,1]
	v_cvt_pk_fp8_f32 v135, v114, v115 op_sel:[0,0,1]
	v_lshl_add_u64 v[112:113], v[138:139], 0, v[128:129]
	v_mad_i64_i32 v[118:119], s[24:25], v136, s48, v[130:131]
	global_store_dwordx2 v[112:113], v[134:135], off
	v_mov_b32_e32 v114, 0
	v_mov_b32_e32 v115, 0
	v_or_b32_e32 v116, 48, v160
	v_ashrrev_i32_e32 v117, 31, v116
	s_waitcnt vmcnt(7)
	v_pk_mul_f32 v[122:123], v[88:89], v[198:199] op_sel_hi:[1,0]
	v_pk_mul_f32 v[126:127], v[84:85], v[198:199] op_sel_hi:[1,0]
	v_pk_mul_f32 v[120:121], v[90:91], v[198:199] op_sel_hi:[1,0]
	v_pk_mul_f32 v[124:125], v[86:87], v[198:199] op_sel_hi:[1,0]
	v_pk_mul_f32 v[132:133], v[80:81], v[198:199] op_sel_hi:[1,0]
	v_pk_mul_f32 v[134:135], v[82:83], v[198:199] op_sel_hi:[1,0]
	v_pk_mul_f32 v[136:137], v[76:77], v[198:199] op_sel_hi:[1,0]
	v_pk_mul_f32 v[112:113], v[78:79], v[198:199] op_sel_hi:[1,0]
	v_pk_mul_f32 v[108:109], v[122:123], v[108:109]
	v_pk_mul_f32 v[104:105], v[126:127], v[104:105]
	v_pk_mul_f32 v[110:111], v[120:121], v[110:111]
	v_pk_mul_f32 v[106:107], v[124:125], v[106:107]
	v_pk_mul_f32 v[98:99], v[112:113], v[98:99]
	v_pk_mul_f32 v[96:97], v[136:137], v[96:97]
	v_pk_mul_f32 v[120:121], v[108:109], s[12:13] op_sel_hi:[1,0]
	v_pk_mul_f32 v[124:125], v[104:105], s[12:13] op_sel_hi:[1,0]
	v_pk_mul_f32 v[122:123], v[106:107], s[12:13] op_sel_hi:[1,0]
	v_pk_mul_f32 v[96:97], v[104:105], v[96:97]
	v_pk_mul_f32 v[98:99], v[106:107], v[98:99]
	v_exp_f32_e32 v104, v120
	v_exp_f32_e32 v106, v124
	v_exp_f32_e32 v105, v121
	v_exp_f32_e32 v107, v125
	v_pk_mul_f32 v[102:103], v[134:135], v[102:103]
	v_pk_mul_f32 v[100:101], v[132:133], v[100:101]
	v_pk_mul_f32 v[112:113], v[110:111], s[12:13] op_sel_hi:[1,0]
	v_pk_mul_f32 v[100:101], v[108:109], v[100:101]
	v_pk_mul_f32 v[102:103], v[110:111], v[102:103]
	v_exp_f32_e32 v108, v112
	v_exp_f32_e32 v109, v113
	v_exp_f32_e32 v110, v122
	v_exp_f32_e32 v111, v123
	v_pk_add_f32 v[104:105], v[104:105], 1.0 op_sel_hi:[1,0]
	v_pk_add_f32 v[106:107], v[106:107], 1.0 op_sel_hi:[1,0]
	v_rcp_f32_e32 v104, v104
	v_rcp_f32_e32 v106, v106
	v_rcp_f32_e32 v105, v105
	v_rcp_f32_e32 v107, v107
	v_pk_add_f32 v[108:109], v[108:109], 1.0 op_sel_hi:[1,0]
	v_pk_add_f32 v[110:111], v[110:111], 1.0 op_sel_hi:[1,0]
	v_rcp_f32_e32 v108, v108
	v_rcp_f32_e32 v110, v110
	v_rcp_f32_e32 v109, v109
	v_rcp_f32_e32 v111, v111
	v_pk_mul_f32 v[100:101], v[100:101], v[104:105]
	v_pk_mul_f32 v[96:97], v[96:97], v[106:107]
	v_cvt_pk_fp8_f32 v114, v100, v101
	v_cvt_pk_fp8_f32 v115, v96, v97
	v_pk_mul_f32 v[96:97], v[102:103], v[108:109]
	v_pk_mul_f32 v[98:99], v[98:99], v[110:111]
	v_cvt_pk_fp8_f32 v114, v96, v97 op_sel:[0,0,1]
	v_cvt_pk_fp8_f32 v115, v98, v99 op_sel:[0,0,1]
	v_lshl_add_u64 v[96:97], v[118:119], 0, v[128:129]
	global_store_dwordx2 v[96:97], v[114:115], off
	v_mov_b32_e32 v98, 0
	v_mov_b32_e32 v99, 0
	s_waitcnt vmcnt(7)
	v_pk_mul_f32 v[102:103], v[88:89], v[200:201] op_sel_hi:[1,0]
	v_pk_mul_f32 v[106:107], v[84:85], v[200:201] op_sel_hi:[1,0]
	v_pk_mul_f32 v[100:101], v[90:91], v[200:201] op_sel_hi:[1,0]
	v_pk_mul_f32 v[104:105], v[86:87], v[200:201] op_sel_hi:[1,0]
	v_pk_mul_f32 v[108:109], v[80:81], v[200:201] op_sel_hi:[1,0]
	v_pk_mul_f32 v[110:111], v[82:83], v[200:201] op_sel_hi:[1,0]
	v_pk_mul_f32 v[112:113], v[76:77], v[200:201] op_sel_hi:[1,0]
	v_pk_mul_f32 v[96:97], v[78:79], v[200:201] op_sel_hi:[1,0]
	v_pk_mul_f32 v[92:93], v[102:103], v[92:93]
	v_pk_mul_f32 v[72:73], v[106:107], v[72:73]
	v_pk_mul_f32 v[94:95], v[100:101], v[94:95]
	v_pk_mul_f32 v[74:75], v[104:105], v[74:75]
	v_pk_mul_f32 v[66:67], v[96:97], v[66:67]
	v_pk_mul_f32 v[64:65], v[112:113], v[64:65]
	v_pk_mul_f32 v[100:101], v[92:93], s[12:13] op_sel_hi:[1,0]
	v_pk_mul_f32 v[104:105], v[72:73], s[12:13] op_sel_hi:[1,0]
	v_pk_mul_f32 v[102:103], v[74:75], s[12:13] op_sel_hi:[1,0]
	v_pk_mul_f32 v[64:65], v[72:73], v[64:65]
	v_pk_mul_f32 v[66:67], v[74:75], v[66:67]
	v_exp_f32_e32 v72, v100
	v_exp_f32_e32 v74, v104
	v_exp_f32_e32 v73, v101
	v_exp_f32_e32 v75, v105
	v_pk_mul_f32 v[70:71], v[110:111], v[70:71]
	v_pk_mul_f32 v[68:69], v[108:109], v[68:69]
	v_pk_mul_f32 v[96:97], v[94:95], s[12:13] op_sel_hi:[1,0]
	v_pk_mul_f32 v[68:69], v[92:93], v[68:69]
	v_pk_mul_f32 v[70:71], v[94:95], v[70:71]
	v_exp_f32_e32 v92, v96
	v_exp_f32_e32 v93, v97
	v_exp_f32_e32 v94, v102
	v_exp_f32_e32 v95, v103
	v_pk_add_f32 v[72:73], v[72:73], 1.0 op_sel_hi:[1,0]
	v_pk_add_f32 v[74:75], v[74:75], 1.0 op_sel_hi:[1,0]
	v_rcp_f32_e32 v72, v72
	v_rcp_f32_e32 v74, v74
	v_rcp_f32_e32 v73, v73
	v_rcp_f32_e32 v75, v75
	v_pk_add_f32 v[92:93], v[92:93], 1.0 op_sel_hi:[1,0]
	v_pk_add_f32 v[94:95], v[94:95], 1.0 op_sel_hi:[1,0]
	v_rcp_f32_e32 v92, v92
	v_rcp_f32_e32 v94, v94
	v_rcp_f32_e32 v93, v93
	v_rcp_f32_e32 v95, v95
	v_pk_mul_f32 v[68:69], v[68:69], v[72:73]
	v_pk_mul_f32 v[64:65], v[64:65], v[74:75]
	v_cvt_pk_fp8_f32 v98, v68, v69
	v_cvt_pk_fp8_f32 v99, v64, v65
	v_pk_mul_f32 v[64:65], v[70:71], v[92:93]
	v_pk_mul_f32 v[66:67], v[66:67], v[94:95]
	v_cvt_pk_fp8_f32 v98, v64, v65 op_sel:[0,0,1]
	v_cvt_pk_fp8_f32 v99, v66, v67 op_sel:[0,0,1]
	v_mad_i64_i32 v[64:65], s[24:25], v116, s48, v[130:131]
	v_lshl_add_u64 v[64:65], v[64:65], 0, v[128:129]
	global_store_dwordx2 v[64:65], v[98:99], off
	v_mov_b32_e32 v66, 0
	v_mov_b32_e32 v67, 0
	v_add_u32_e32 v98, 0x80, v160
	s_waitcnt vmcnt(7)
	v_pk_mul_f32 v[70:71], v[88:89], v[202:203] op_sel_hi:[1,0]
	v_pk_mul_f32 v[74:75], v[84:85], v[202:203] op_sel_hi:[1,0]
	v_pk_mul_f32 v[68:69], v[90:91], v[202:203] op_sel_hi:[1,0]
	v_pk_mul_f32 v[72:73], v[86:87], v[202:203] op_sel_hi:[1,0]
	v_pk_mul_f32 v[92:93], v[80:81], v[202:203] op_sel_hi:[1,0]
	v_pk_mul_f32 v[94:95], v[82:83], v[202:203] op_sel_hi:[1,0]
	v_pk_mul_f32 v[96:97], v[76:77], v[202:203] op_sel_hi:[1,0]
	v_pk_mul_f32 v[64:65], v[78:79], v[202:203] op_sel_hi:[1,0]
	v_pk_mul_f32 v[60:61], v[70:71], v[60:61]
	v_pk_mul_f32 v[56:57], v[74:75], v[56:57]
	v_pk_mul_f32 v[62:63], v[68:69], v[62:63]
	v_pk_mul_f32 v[58:59], v[72:73], v[58:59]
	v_pk_mul_f32 v[50:51], v[64:65], v[50:51]
	v_pk_mul_f32 v[48:49], v[96:97], v[48:49]
	v_pk_mul_f32 v[68:69], v[60:61], s[12:13] op_sel_hi:[1,0]
	v_pk_mul_f32 v[72:73], v[56:57], s[12:13] op_sel_hi:[1,0]
	v_pk_mul_f32 v[70:71], v[58:59], s[12:13] op_sel_hi:[1,0]
	v_pk_mul_f32 v[48:49], v[56:57], v[48:49]
	v_pk_mul_f32 v[50:51], v[58:59], v[50:51]
	v_exp_f32_e32 v56, v68
	v_exp_f32_e32 v58, v72
	v_exp_f32_e32 v57, v69
	v_exp_f32_e32 v59, v73
	v_pk_mul_f32 v[54:55], v[94:95], v[54:55]
	v_pk_mul_f32 v[52:53], v[92:93], v[52:53]
	v_pk_mul_f32 v[64:65], v[62:63], s[12:13] op_sel_hi:[1,0]
	v_pk_mul_f32 v[52:53], v[60:61], v[52:53]
	v_pk_mul_f32 v[54:55], v[62:63], v[54:55]
	v_exp_f32_e32 v60, v64
	v_exp_f32_e32 v61, v65
	v_exp_f32_e32 v62, v70
	v_exp_f32_e32 v63, v71
	v_pk_add_f32 v[56:57], v[56:57], 1.0 op_sel_hi:[1,0]
	v_pk_add_f32 v[58:59], v[58:59], 1.0 op_sel_hi:[1,0]
	v_rcp_f32_e32 v56, v56
	v_rcp_f32_e32 v58, v58
	v_rcp_f32_e32 v57, v57
	v_rcp_f32_e32 v59, v59
	v_pk_add_f32 v[60:61], v[60:61], 1.0 op_sel_hi:[1,0]
	v_pk_add_f32 v[62:63], v[62:63], 1.0 op_sel_hi:[1,0]
	v_rcp_f32_e32 v60, v60
	v_rcp_f32_e32 v62, v62
	v_rcp_f32_e32 v61, v61
	v_rcp_f32_e32 v63, v63
	v_pk_mul_f32 v[52:53], v[52:53], v[56:57]
	v_pk_mul_f32 v[48:49], v[48:49], v[58:59]
	v_cvt_pk_fp8_f32 v66, v52, v53
	v_cvt_pk_fp8_f32 v67, v48, v49
	v_pk_mul_f32 v[48:49], v[54:55], v[60:61]
	v_pk_mul_f32 v[50:51], v[50:51], v[62:63]
	v_cvt_pk_fp8_f32 v66, v48, v49 op_sel:[0,0,1]
	v_cvt_pk_fp8_f32 v67, v50, v51 op_sel:[0,0,1]
	v_mad_i64_i32 v[48:49], s[24:25], v98, s48, v[130:131]
	v_lshl_add_u64 v[48:49], v[48:49], 0, v[128:129]
	global_store_dwordx2 v[48:49], v[66:67], off
	v_mov_b32_e32 v50, 0
	v_mov_b32_e32 v51, 0
	v_add_u32_e32 v66, 0x90, v160
	s_waitcnt vmcnt(7)
	v_pk_mul_f32 v[54:55], v[88:89], v[204:205] op_sel_hi:[1,0]
	v_pk_mul_f32 v[58:59], v[84:85], v[204:205] op_sel_hi:[1,0]
	v_pk_mul_f32 v[52:53], v[90:91], v[204:205] op_sel_hi:[1,0]
	v_pk_mul_f32 v[56:57], v[86:87], v[204:205] op_sel_hi:[1,0]
	v_pk_mul_f32 v[60:61], v[80:81], v[204:205] op_sel_hi:[1,0]
	v_pk_mul_f32 v[62:63], v[82:83], v[204:205] op_sel_hi:[1,0]
	v_pk_mul_f32 v[64:65], v[76:77], v[204:205] op_sel_hi:[1,0]
	v_pk_mul_f32 v[48:49], v[78:79], v[204:205] op_sel_hi:[1,0]
	v_pk_mul_f32 v[44:45], v[54:55], v[44:45]
	v_pk_mul_f32 v[40:41], v[58:59], v[40:41]
	v_pk_mul_f32 v[46:47], v[52:53], v[46:47]
	v_pk_mul_f32 v[42:43], v[56:57], v[42:43]
	v_pk_mul_f32 v[34:35], v[48:49], v[34:35]
	v_pk_mul_f32 v[32:33], v[64:65], v[32:33]
	v_pk_mul_f32 v[52:53], v[44:45], s[12:13] op_sel_hi:[1,0]
	v_pk_mul_f32 v[56:57], v[40:41], s[12:13] op_sel_hi:[1,0]
	v_pk_mul_f32 v[54:55], v[42:43], s[12:13] op_sel_hi:[1,0]
	v_pk_mul_f32 v[32:33], v[40:41], v[32:33]
	v_pk_mul_f32 v[34:35], v[42:43], v[34:35]
	v_exp_f32_e32 v40, v52
	v_exp_f32_e32 v42, v56
	v_exp_f32_e32 v41, v53
	v_exp_f32_e32 v43, v57
	v_pk_mul_f32 v[38:39], v[62:63], v[38:39]
	v_pk_mul_f32 v[36:37], v[60:61], v[36:37]
	v_pk_mul_f32 v[48:49], v[46:47], s[12:13] op_sel_hi:[1,0]
	v_pk_mul_f32 v[36:37], v[44:45], v[36:37]
	v_pk_mul_f32 v[38:39], v[46:47], v[38:39]
	v_exp_f32_e32 v44, v48
	v_exp_f32_e32 v45, v49
	v_exp_f32_e32 v46, v54
	v_exp_f32_e32 v47, v55
	v_pk_add_f32 v[40:41], v[40:41], 1.0 op_sel_hi:[1,0]
	v_pk_add_f32 v[42:43], v[42:43], 1.0 op_sel_hi:[1,0]
	v_rcp_f32_e32 v40, v40
	v_rcp_f32_e32 v42, v42
	v_rcp_f32_e32 v41, v41
	v_rcp_f32_e32 v43, v43
	v_pk_add_f32 v[44:45], v[44:45], 1.0 op_sel_hi:[1,0]
	v_pk_add_f32 v[46:47], v[46:47], 1.0 op_sel_hi:[1,0]
	v_rcp_f32_e32 v44, v44
	v_rcp_f32_e32 v46, v46
	v_rcp_f32_e32 v45, v45
	v_rcp_f32_e32 v47, v47
	v_pk_mul_f32 v[36:37], v[36:37], v[40:41]
	v_pk_mul_f32 v[32:33], v[32:33], v[42:43]
	v_cvt_pk_fp8_f32 v50, v36, v37
	v_cvt_pk_fp8_f32 v51, v32, v33
	v_pk_mul_f32 v[32:33], v[38:39], v[44:45]
	v_pk_mul_f32 v[34:35], v[34:35], v[46:47]
	v_cvt_pk_fp8_f32 v50, v32, v33 op_sel:[0,0,1]
	v_cvt_pk_fp8_f32 v51, v34, v35 op_sel:[0,0,1]
	v_mad_i64_i32 v[32:33], s[24:25], v66, s48, v[130:131]
	v_lshl_add_u64 v[32:33], v[32:33], 0, v[128:129]
	global_store_dwordx2 v[32:33], v[50:51], off
	v_mov_b32_e32 v34, 0
	v_mov_b32_e32 v35, 0
	v_add_u32_e32 v50, 0xa0, v160
	s_waitcnt vmcnt(7)
	v_pk_mul_f32 v[38:39], v[88:89], v[206:207] op_sel_hi:[1,0]
	v_pk_mul_f32 v[42:43], v[84:85], v[206:207] op_sel_hi:[1,0]
	v_pk_mul_f32 v[36:37], v[90:91], v[206:207] op_sel_hi:[1,0]
	v_pk_mul_f32 v[40:41], v[86:87], v[206:207] op_sel_hi:[1,0]
	v_pk_mul_f32 v[44:45], v[80:81], v[206:207] op_sel_hi:[1,0]
	v_pk_mul_f32 v[46:47], v[82:83], v[206:207] op_sel_hi:[1,0]
	v_pk_mul_f32 v[48:49], v[76:77], v[206:207] op_sel_hi:[1,0]
	v_pk_mul_f32 v[32:33], v[78:79], v[206:207] op_sel_hi:[1,0]
	v_pk_mul_f32 v[28:29], v[38:39], v[28:29]
	v_pk_mul_f32 v[24:25], v[42:43], v[24:25]
	v_pk_mul_f32 v[30:31], v[36:37], v[30:31]
	v_pk_mul_f32 v[26:27], v[40:41], v[26:27]
	v_pk_mul_f32 v[18:19], v[32:33], v[18:19]
	v_pk_mul_f32 v[16:17], v[48:49], v[16:17]
	v_pk_mul_f32 v[36:37], v[28:29], s[12:13] op_sel_hi:[1,0]
	v_pk_mul_f32 v[40:41], v[24:25], s[12:13] op_sel_hi:[1,0]
	v_pk_mul_f32 v[38:39], v[26:27], s[12:13] op_sel_hi:[1,0]
	v_pk_mul_f32 v[16:17], v[24:25], v[16:17]
	v_pk_mul_f32 v[18:19], v[26:27], v[18:19]
	v_exp_f32_e32 v24, v36
	v_exp_f32_e32 v26, v40
	v_exp_f32_e32 v25, v37
	v_exp_f32_e32 v27, v41
	v_pk_mul_f32 v[22:23], v[46:47], v[22:23]
	v_pk_mul_f32 v[20:21], v[44:45], v[20:21]
	v_pk_mul_f32 v[32:33], v[30:31], s[12:13] op_sel_hi:[1,0]
	v_pk_mul_f32 v[20:21], v[28:29], v[20:21]
	v_pk_mul_f32 v[22:23], v[30:31], v[22:23]
	v_exp_f32_e32 v28, v32
	v_exp_f32_e32 v29, v33
	v_exp_f32_e32 v30, v38
	v_exp_f32_e32 v31, v39
	v_pk_add_f32 v[24:25], v[24:25], 1.0 op_sel_hi:[1,0]
	v_pk_add_f32 v[26:27], v[26:27], 1.0 op_sel_hi:[1,0]
	v_rcp_f32_e32 v24, v24
	v_rcp_f32_e32 v26, v26
	v_rcp_f32_e32 v25, v25
	v_rcp_f32_e32 v27, v27
	v_pk_add_f32 v[28:29], v[28:29], 1.0 op_sel_hi:[1,0]
	v_pk_add_f32 v[30:31], v[30:31], 1.0 op_sel_hi:[1,0]
	v_rcp_f32_e32 v28, v28
	v_rcp_f32_e32 v30, v30
	v_rcp_f32_e32 v29, v29
	v_rcp_f32_e32 v31, v31
	v_pk_mul_f32 v[20:21], v[20:21], v[24:25]
	v_pk_mul_f32 v[16:17], v[16:17], v[26:27]
	v_cvt_pk_fp8_f32 v34, v20, v21
	v_cvt_pk_fp8_f32 v35, v16, v17
	v_pk_mul_f32 v[16:17], v[22:23], v[28:29]
	v_pk_mul_f32 v[18:19], v[18:19], v[30:31]
	v_cvt_pk_fp8_f32 v34, v16, v17 op_sel:[0,0,1]
	v_cvt_pk_fp8_f32 v35, v18, v19 op_sel:[0,0,1]
	v_mad_i64_i32 v[16:17], s[24:25], v50, s48, v[130:131]
	v_lshl_add_u64 v[16:17], v[16:17], 0, v[128:129]
	global_store_dwordx2 v[16:17], v[34:35], off
	v_mov_b32_e32 v18, 0
	v_mov_b32_e32 v19, 0
	v_add_u32_e32 v34, 0xb0, v160
	s_waitcnt vmcnt(7)
	v_pk_mul_f32 v[22:23], v[88:89], v[208:209] op_sel_hi:[1,0]
	v_pk_mul_f32 v[26:27], v[84:85], v[208:209] op_sel_hi:[1,0]
	v_pk_mul_f32 v[20:21], v[90:91], v[208:209] op_sel_hi:[1,0]
	v_pk_mul_f32 v[24:25], v[86:87], v[208:209] op_sel_hi:[1,0]
	v_pk_mul_f32 v[28:29], v[80:81], v[208:209] op_sel_hi:[1,0]
	v_pk_mul_f32 v[30:31], v[82:83], v[208:209] op_sel_hi:[1,0]
	v_pk_mul_f32 v[32:33], v[76:77], v[208:209] op_sel_hi:[1,0]
	v_pk_mul_f32 v[16:17], v[78:79], v[208:209] op_sel_hi:[1,0]
	v_pk_mul_f32 v[12:13], v[22:23], v[12:13]
	v_pk_mul_f32 v[8:9], v[26:27], v[8:9]
	v_pk_mul_f32 v[14:15], v[20:21], v[14:15]
	v_pk_mul_f32 v[10:11], v[24:25], v[10:11]
	v_pk_mul_f32 v[2:3], v[16:17], v[2:3]
	v_pk_mul_f32 v[0:1], v[32:33], v[0:1]
	v_pk_mul_f32 v[20:21], v[12:13], s[12:13] op_sel_hi:[1,0]
	v_pk_mul_f32 v[24:25], v[8:9], s[12:13] op_sel_hi:[1,0]
	v_pk_mul_f32 v[22:23], v[10:11], s[12:13] op_sel_hi:[1,0]
	v_pk_mul_f32 v[0:1], v[8:9], v[0:1]
	v_pk_mul_f32 v[2:3], v[10:11], v[2:3]
	v_exp_f32_e32 v8, v20
	v_exp_f32_e32 v10, v24
	v_exp_f32_e32 v9, v21
	v_exp_f32_e32 v11, v25
	v_pk_mul_f32 v[6:7], v[30:31], v[6:7]
	v_pk_mul_f32 v[4:5], v[28:29], v[4:5]
	v_pk_mul_f32 v[16:17], v[14:15], s[12:13] op_sel_hi:[1,0]
	v_pk_mul_f32 v[4:5], v[12:13], v[4:5]
	v_pk_mul_f32 v[6:7], v[14:15], v[6:7]
	v_exp_f32_e32 v12, v16
	v_exp_f32_e32 v13, v17
	v_exp_f32_e32 v14, v22
	v_exp_f32_e32 v15, v23
	v_pk_add_f32 v[8:9], v[8:9], 1.0 op_sel_hi:[1,0]
	v_pk_add_f32 v[10:11], v[10:11], 1.0 op_sel_hi:[1,0]
	v_rcp_f32_e32 v8, v8
	v_rcp_f32_e32 v10, v10
	v_rcp_f32_e32 v9, v9
	v_rcp_f32_e32 v11, v11
	v_pk_add_f32 v[12:13], v[12:13], 1.0 op_sel_hi:[1,0]
	v_pk_add_f32 v[14:15], v[14:15], 1.0 op_sel_hi:[1,0]
	v_rcp_f32_e32 v12, v12
	v_rcp_f32_e32 v14, v14
	v_rcp_f32_e32 v13, v13
	v_rcp_f32_e32 v15, v15
	v_pk_mul_f32 v[4:5], v[4:5], v[8:9]
	v_pk_mul_f32 v[0:1], v[0:1], v[10:11]
	v_cvt_pk_fp8_f32 v18, v4, v5
	v_cvt_pk_fp8_f32 v19, v0, v1
	v_pk_mul_f32 v[0:1], v[6:7], v[12:13]
	v_pk_mul_f32 v[2:3], v[2:3], v[14:15]
	v_cvt_pk_fp8_f32 v18, v0, v1 op_sel:[0,0,1]
	v_cvt_pk_fp8_f32 v19, v2, v3 op_sel:[0,0,1]
	v_mad_i64_i32 v[0:1], s[24:25], v34, s48, v[130:131]
	v_lshl_add_u64 v[0:1], v[0:1], 0, v[128:129]
	global_store_dwordx2 v[0:1], v[18:19], off
	s_cbranch_vccnz .LBB0_490
	s_andn2_b64 vcc, exec, s[4:5]
	s_cbranch_vccnz .LBB0_489
	s_barrier
	s_branch .LBB0_489

.LBB0_1847:
	s_add_u32 s28, s28, 0x40080
	s_addc_u32 s29, s29, 0
	s_add_u32 s17, s30, 0x100
	s_addc_u32 s19, s31, 0
	s_mov_b32 s69, -2
	ds_read_b128 v[76:79], v163
	ds_read_b128 v[80:83], v163 offset:1024
	ds_read_b128 v[84:87], v163 offset:2048
	ds_read_b128 v[88:91], v163 offset:3072
	ds_read_b128 v[158:161], v164
	ds_read_b128 v[166:169], v164 offset:1024
	ds_read_b128 v[170:173], v164 offset:2048
	ds_read_b128 v[174:177], v164 offset:3072
	s_add_u32 s30, s28, 0xfffc0080
	s_addc_u32 s31, s29, -1
	s_cmp_eq_u32 s69, 12
	s_cselect_b32 s35, s21, s31
	s_cselect_b32 s34, s20, s30
	s_cselect_b32 s31, s23, s19
	s_cselect_b32 s30, s22, s17
	v_lshl_add_u64 v[210:211], s[28:29], 0, v[152:153]
	s_add_i32 m0, s25, 0xc000
	ds_read_b128 v[178:181], v165
	ds_read_b128 v[182:185], v165 offset:1024
	ds_read_b128 v[186:189], v165 offset:2048
	ds_read_b128 v[190:193], v165 offset:3072
	ds_read_b128 v[194:197], v165 offset:4096
	ds_read_b128 v[198:201], v165 offset:5120
	ds_read_b128 v[202:205], v165 offset:6144
	ds_read_b128 v[206:209], v165 offset:7168
	global_load_lds_dwordx4 v[210:211], off
	v_lshl_add_u64 v[210:211], s[28:29], 0, v[154:155]
	s_add_i32 m0, s25, 0xe000
	s_nop 0
	global_load_lds_dwordx4 v[210:211], off
	s_waitcnt vmcnt(8)
	s_waitcnt lgkmcnt(0)
	s_barrier
	s_setprio 1
	s_waitcnt lgkmcnt(0)
	v_mfma_i32_16x16x64_i8 v[140:143], v[76:79], v[178:181], 0
	v_mfma_i32_16x16x64_i8 v[136:139], v[84:87], v[178:181], 0
	v_mfma_i32_16x16x64_i8 v[124:127], v[76:79], v[186:189], 0
	v_mfma_i32_16x16x64_i8 v[120:123], v[84:87], v[186:189], 0
	v_mfma_i32_16x16x64_i8 v[108:111], v[76:79], v[194:197], 0
	v_mfma_i32_16x16x64_i8 v[104:107], v[84:87], v[194:197], 0
	v_mfma_i32_16x16x64_i8 v[92:95], v[76:79], v[202:205], 0
	v_mfma_i32_16x16x64_i8 v[72:75], v[84:87], v[202:205], 0
	v_mfma_i32_16x16x64_i8 v[140:143], v[80:83], v[182:185], v[140:143]
	v_mfma_i32_16x16x64_i8 v[136:139], v[88:91], v[182:185], v[136:139]
	v_mfma_i32_16x16x64_i8 v[124:127], v[80:83], v[190:193], v[124:127]
	v_mfma_i32_16x16x64_i8 v[120:123], v[88:91], v[190:193], v[120:123]
	v_mfma_i32_16x16x64_i8 v[108:111], v[80:83], v[198:201], v[108:111]
	v_mfma_i32_16x16x64_i8 v[104:107], v[88:91], v[198:201], v[104:107]
	v_mfma_i32_16x16x64_i8 v[92:95], v[80:83], v[206:209], v[92:95]
	v_mfma_i32_16x16x64_i8 v[72:75], v[88:91], v[206:209], v[72:75]
	s_setprio 0
	s_setprio 1
	v_mfma_i32_16x16x64_i8 v[132:135], v[158:161], v[178:181], 0
	v_mfma_i32_16x16x64_i8 v[128:131], v[170:173], v[178:181], 0
	v_mfma_i32_16x16x64_i8 v[116:119], v[158:161], v[186:189], 0
	v_mfma_i32_16x16x64_i8 v[112:115], v[170:173], v[186:189], 0
	v_mfma_i32_16x16x64_i8 v[100:103], v[158:161], v[194:197], 0
	v_mfma_i32_16x16x64_i8 v[96:99], v[170:173], v[194:197], 0
	v_mfma_i32_16x16x64_i8 v[68:71], v[158:161], v[202:205], 0
	v_mfma_i32_16x16x64_i8 v[64:67], v[170:173], v[202:205], 0
	v_mfma_i32_16x16x64_i8 v[132:135], v[166:169], v[182:185], v[132:135]
	v_mfma_i32_16x16x64_i8 v[128:131], v[174:177], v[182:185], v[128:131]
	v_mfma_i32_16x16x64_i8 v[116:119], v[166:169], v[190:193], v[116:119]
	v_mfma_i32_16x16x64_i8 v[112:115], v[174:177], v[190:193], v[112:115]
	v_mfma_i32_16x16x64_i8 v[100:103], v[166:169], v[198:201], v[100:103]
	v_mfma_i32_16x16x64_i8 v[96:99], v[174:177], v[198:201], v[96:99]
	v_mfma_i32_16x16x64_i8 v[68:71], v[166:169], v[206:209], v[68:71]
	v_mfma_i32_16x16x64_i8 v[64:67], v[174:177], v[206:209], v[64:67]
	s_setprio 0
	s_barrier
	s_add_i32 s70, s60, s39
	v_lshl_add_u64 v[210:211], s[30:31], 0, v[148:149]
	s_mov_b32 m0, s70
	ds_read_b128 v[178:181], v165 offset:16384
	ds_read_b128 v[182:185], v165 offset:17408
	ds_read_b128 v[186:189], v165 offset:18432
	ds_read_b128 v[190:193], v165 offset:19456
	ds_read_b128 v[194:197], v165 offset:20480
	ds_read_b128 v[198:201], v165 offset:21504
	ds_read_b128 v[202:205], v165 offset:22528
	ds_read_b128 v[206:209], v165 offset:23552
	global_load_lds_dwordx4 v[210:211], off
	s_add_i32 m0, s70, 0x2000
	s_add_u32 s70, s30, 0x40000
	v_lshl_add_u64 v[212:213], s[30:31], 0, v[144:145]
	s_addc_u32 s71, s31, 0
	s_add_i32 s72, s61, s39
	global_load_lds_dwordx4 v[212:213], off
	v_lshl_add_u64 v[214:215], s[70:71], 0, v[148:149]
	s_mov_b32 m0, s72
	v_lshl_add_u64 v[216:217], s[34:35], 0, v[146:147]
	global_load_lds_dwordx4 v[214:215], off
	v_lshl_add_u64 v[214:215], s[70:71], 0, v[144:145]
	s_add_i32 m0, s72, 0x2000
	s_nop 0
	global_load_lds_dwordx4 v[214:215], off
	v_lshl_add_u64 v[214:215], s[34:35], 0, v[150:151]
	s_mov_b32 m0, s25
	s_nop 0
	global_load_lds_dwordx4 v[214:215], off
	s_mov_b32 m0, s27
	s_nop 0
	global_load_lds_dwordx4 v[216:217], off
	s_waitcnt vmcnt(8)
	s_waitcnt lgkmcnt(0)
	s_barrier
	s_setprio 1
	s_waitcnt lgkmcnt(0)
	v_mfma_i32_16x16x64_i8 v[60:63], v[76:79], v[178:181], 0
	v_mfma_i32_16x16x64_i8 v[56:59], v[84:87], v[178:181], 0
	v_mfma_i32_16x16x64_i8 v[44:47], v[76:79], v[186:189], 0
	v_mfma_i32_16x16x64_i8 v[40:43], v[84:87], v[186:189], 0
	v_mfma_i32_16x16x64_i8 v[28:31], v[76:79], v[194:197], 0
	v_mfma_i32_16x16x64_i8 v[24:27], v[84:87], v[194:197], 0
	v_mfma_i32_16x16x64_i8 v[12:15], v[76:79], v[202:205], 0
	v_mfma_i32_16x16x64_i8 v[8:11], v[84:87], v[202:205], 0
	v_mfma_i32_16x16x64_i8 v[60:63], v[80:83], v[182:185], v[60:63]
	v_mfma_i32_16x16x64_i8 v[56:59], v[88:91], v[182:185], v[56:59]
	v_mfma_i32_16x16x64_i8 v[44:47], v[80:83], v[190:193], v[44:47]
	v_mfma_i32_16x16x64_i8 v[40:43], v[88:91], v[190:193], v[40:43]
	v_mfma_i32_16x16x64_i8 v[28:31], v[80:83], v[198:201], v[28:31]
	v_mfma_i32_16x16x64_i8 v[24:27], v[88:91], v[198:201], v[24:27]
	v_mfma_i32_16x16x64_i8 v[12:15], v[80:83], v[206:209], v[12:15]
	v_mfma_i32_16x16x64_i8 v[8:11], v[88:91], v[206:209], v[8:11]
	s_setprio 0
	s_setprio 1
	v_mfma_i32_16x16x64_i8 v[52:55], v[158:161], v[178:181], 0
	v_mfma_i32_16x16x64_i8 v[48:51], v[170:173], v[178:181], 0
	v_mfma_i32_16x16x64_i8 v[36:39], v[158:161], v[186:189], 0
	v_mfma_i32_16x16x64_i8 v[32:35], v[170:173], v[186:189], 0
	v_mfma_i32_16x16x64_i8 v[20:23], v[158:161], v[194:197], 0
	v_mfma_i32_16x16x64_i8 v[16:19], v[170:173], v[194:197], 0
	v_mfma_i32_16x16x64_i8 v[4:7], v[158:161], v[202:205], 0
	v_mfma_i32_16x16x64_i8 v[0:3], v[170:173], v[202:205], 0
	v_mfma_i32_16x16x64_i8 v[52:55], v[166:169], v[182:185], v[52:55]
	v_mfma_i32_16x16x64_i8 v[48:51], v[174:177], v[182:185], v[48:51]
	v_mfma_i32_16x16x64_i8 v[36:39], v[166:169], v[190:193], v[36:39]
	v_mfma_i32_16x16x64_i8 v[32:35], v[174:177], v[190:193], v[32:35]
	v_mfma_i32_16x16x64_i8 v[20:23], v[166:169], v[198:201], v[20:23]
	v_mfma_i32_16x16x64_i8 v[16:19], v[174:177], v[198:201], v[16:19]
	v_mfma_i32_16x16x64_i8 v[4:7], v[166:169], v[206:209], v[4:7]
	v_mfma_i32_16x16x64_i8 v[0:3], v[174:177], v[206:209], v[0:3]
	s_setprio 0
	s_barrier
	s_add_i32 s70, 0, 0x18000
	s_add_i32 s71, 0, 0x1c000
	v_add_u32_e32 v88, s70, v162
	v_add_u32_e32 v174, s71, v162
	ds_read_b128 v[76:79], v88
	ds_read_b128 v[80:83], v88 offset:1024
	ds_read_b128 v[84:87], v88 offset:2048
	ds_read_b128 v[88:91], v88 offset:3072
	ds_read_b128 v[158:161], v174
	ds_read_b128 v[166:169], v174 offset:1024
	ds_read_b128 v[170:173], v174 offset:2048
	ds_read_b128 v[174:177], v174 offset:3072
	s_add_u32 s34, s34, 0x40000
	s_addc_u32 s35, s35, 0
	s_mov_b32 m0, s50
	v_lshl_add_u64 v[218:219], s[34:35], 0, v[150:151]
	ds_read_b128 v[178:181], v165 offset:32768
	ds_read_b128 v[182:185], v165 offset:33792
	ds_read_b128 v[186:189], v165 offset:34816
	ds_read_b128 v[190:193], v165 offset:35840
	ds_read_b128 v[194:197], v165 offset:36864
	ds_read_b128 v[198:201], v165 offset:37888
	ds_read_b128 v[202:205], v165 offset:38912
	ds_read_b128 v[206:209], v165 offset:39936
	global_load_lds_dwordx4 v[218:219], off
	v_lshl_add_u64 v[218:219], s[34:35], 0, v[146:147]
	s_mov_b32 m0, s51
	s_nop 0
	global_load_lds_dwordx4 v[218:219], off
	s_waitcnt vmcnt(8)
	s_waitcnt lgkmcnt(0)
	s_barrier
	s_setprio 1
	s_waitcnt lgkmcnt(0)
	v_mfma_i32_16x16x64_i8 v[140:143], v[76:79], v[178:181], v[140:143]
	v_mfma_i32_16x16x64_i8 v[136:139], v[84:87], v[178:181], v[136:139]
	v_mfma_i32_16x16x64_i8 v[124:127], v[76:79], v[186:189], v[124:127]
	v_mfma_i32_16x16x64_i8 v[120:123], v[84:87], v[186:189], v[120:123]
	v_mfma_i32_16x16x64_i8 v[108:111], v[76:79], v[194:197], v[108:111]
	v_mfma_i32_16x16x64_i8 v[104:107], v[84:87], v[194:197], v[104:107]
	v_mfma_i32_16x16x64_i8 v[92:95], v[76:79], v[202:205], v[92:95]
	v_mfma_i32_16x16x64_i8 v[72:75], v[84:87], v[202:205], v[72:75]
	v_mfma_i32_16x16x64_i8 v[140:143], v[80:83], v[182:185], v[140:143]
	v_mfma_i32_16x16x64_i8 v[136:139], v[88:91], v[182:185], v[136:139]
	v_mfma_i32_16x16x64_i8 v[124:127], v[80:83], v[190:193], v[124:127]
	v_mfma_i32_16x16x64_i8 v[120:123], v[88:91], v[190:193], v[120:123]
	v_mfma_i32_16x16x64_i8 v[108:111], v[80:83], v[198:201], v[108:111]
	v_mfma_i32_16x16x64_i8 v[104:107], v[88:91], v[198:201], v[104:107]
	v_mfma_i32_16x16x64_i8 v[92:95], v[80:83], v[206:209], v[92:95]
	v_mfma_i32_16x16x64_i8 v[72:75], v[88:91], v[206:209], v[72:75]
	s_setprio 0
	s_setprio 1
	v_mfma_i32_16x16x64_i8 v[132:135], v[158:161], v[178:181], v[132:135]
	v_mfma_i32_16x16x64_i8 v[128:131], v[170:173], v[178:181], v[128:131]
	v_mfma_i32_16x16x64_i8 v[116:119], v[158:161], v[186:189], v[116:119]
	v_mfma_i32_16x16x64_i8 v[112:115], v[170:173], v[186:189], v[112:115]
	v_mfma_i32_16x16x64_i8 v[100:103], v[158:161], v[194:197], v[100:103]
	v_mfma_i32_16x16x64_i8 v[96:99], v[170:173], v[194:197], v[96:99]
	v_mfma_i32_16x16x64_i8 v[68:71], v[158:161], v[202:205], v[68:71]
	v_mfma_i32_16x16x64_i8 v[64:67], v[170:173], v[202:205], v[64:67]
	v_mfma_i32_16x16x64_i8 v[132:135], v[166:169], v[182:185], v[132:135]
	v_mfma_i32_16x16x64_i8 v[128:131], v[174:177], v[182:185], v[128:131]
	v_mfma_i32_16x16x64_i8 v[116:119], v[166:169], v[190:193], v[116:119]
	v_mfma_i32_16x16x64_i8 v[112:115], v[174:177], v[190:193], v[112:115]
	v_mfma_i32_16x16x64_i8 v[100:103], v[166:169], v[198:201], v[100:103]
	v_mfma_i32_16x16x64_i8 v[96:99], v[174:177], v[198:201], v[96:99]
	v_mfma_i32_16x16x64_i8 v[68:71], v[166:169], v[206:209], v[68:71]
	v_mfma_i32_16x16x64_i8 v[64:67], v[174:177], v[206:209], v[64:67]
	s_setprio 0
	s_barrier
	s_add_i32 s34, s70, s39
	v_lshl_add_u64 v[210:211], v[210:211], 0, s[12:13]
	s_mov_b32 m0, s34
	ds_read_b128 v[178:181], v165 offset:49152
	ds_read_b128 v[182:185], v165 offset:50176
	ds_read_b128 v[186:189], v165 offset:51200
	ds_read_b128 v[190:193], v165 offset:52224
	ds_read_b128 v[194:197], v165 offset:53248
	ds_read_b128 v[198:201], v165 offset:54272
	ds_read_b128 v[202:205], v165 offset:55296
	ds_read_b128 v[206:209], v165 offset:56320
	global_load_lds_dwordx4 v[210:211], off
	s_add_i32 m0, s34, 0x2000
	s_add_u32 s30, s30, 0x40080
	v_lshl_add_u64 v[210:211], v[212:213], 0, s[12:13]
	s_addc_u32 s31, s31, 0
	s_add_i32 s34, s71, s39
	global_load_lds_dwordx4 v[210:211], off
	v_lshl_add_u64 v[210:211], s[30:31], 0, v[148:149]
	s_mov_b32 m0, s34
	s_nop 0
	global_load_lds_dwordx4 v[210:211], off
	v_lshl_add_u64 v[210:211], s[30:31], 0, v[144:145]
	s_add_i32 m0, s34, 0x2000
	s_nop 0
	global_load_lds_dwordx4 v[210:211], off
	v_lshl_add_u64 v[210:211], v[214:215], 0, s[12:13]
	s_mov_b32 m0, s58
	s_nop 0
	global_load_lds_dwordx4 v[210:211], off
	v_lshl_add_u64 v[210:211], v[216:217], 0, s[12:13]
	s_mov_b32 m0, s59
	s_nop 0
	global_load_lds_dwordx4 v[210:211], off
	s_waitcnt vmcnt(8)
	s_waitcnt lgkmcnt(0)
	s_barrier
	s_setprio 1
	s_waitcnt lgkmcnt(0)
	v_mfma_i32_16x16x64_i8 v[60:63], v[76:79], v[178:181], v[60:63]
	v_mfma_i32_16x16x64_i8 v[56:59], v[84:87], v[178:181], v[56:59]
	v_mfma_i32_16x16x64_i8 v[44:47], v[76:79], v[186:189], v[44:47]
	v_mfma_i32_16x16x64_i8 v[40:43], v[84:87], v[186:189], v[40:43]
	v_mfma_i32_16x16x64_i8 v[28:31], v[76:79], v[194:197], v[28:31]
	v_mfma_i32_16x16x64_i8 v[24:27], v[84:87], v[194:197], v[24:27]
	v_mfma_i32_16x16x64_i8 v[12:15], v[76:79], v[202:205], v[12:15]
	v_mfma_i32_16x16x64_i8 v[8:11], v[84:87], v[202:205], v[8:11]
	v_mfma_i32_16x16x64_i8 v[60:63], v[80:83], v[182:185], v[60:63]
	v_mfma_i32_16x16x64_i8 v[56:59], v[88:91], v[182:185], v[56:59]
	v_mfma_i32_16x16x64_i8 v[44:47], v[80:83], v[190:193], v[44:47]
	v_mfma_i32_16x16x64_i8 v[40:43], v[88:91], v[190:193], v[40:43]
	v_mfma_i32_16x16x64_i8 v[28:31], v[80:83], v[198:201], v[28:31]
	v_mfma_i32_16x16x64_i8 v[24:27], v[88:91], v[198:201], v[24:27]
	v_mfma_i32_16x16x64_i8 v[12:15], v[80:83], v[206:209], v[12:15]
	v_mfma_i32_16x16x64_i8 v[8:11], v[88:91], v[206:209], v[8:11]
	s_setprio 0
	s_setprio 1
	v_mfma_i32_16x16x64_i8 v[52:55], v[158:161], v[178:181], v[52:55]
	v_mfma_i32_16x16x64_i8 v[48:51], v[170:173], v[178:181], v[48:51]
	v_mfma_i32_16x16x64_i8 v[36:39], v[158:161], v[186:189], v[36:39]
	v_mfma_i32_16x16x64_i8 v[32:35], v[170:173], v[186:189], v[32:35]
	v_mfma_i32_16x16x64_i8 v[20:23], v[158:161], v[194:197], v[20:23]
	v_mfma_i32_16x16x64_i8 v[16:19], v[170:173], v[194:197], v[16:19]
	v_mfma_i32_16x16x64_i8 v[4:7], v[158:161], v[202:205], v[4:7]
	v_mfma_i32_16x16x64_i8 v[0:3], v[170:173], v[202:205], v[0:3]
	v_mfma_i32_16x16x64_i8 v[52:55], v[166:169], v[182:185], v[52:55]
	v_mfma_i32_16x16x64_i8 v[48:51], v[174:177], v[182:185], v[48:51]
	v_mfma_i32_16x16x64_i8 v[36:39], v[166:169], v[190:193], v[36:39]
	v_mfma_i32_16x16x64_i8 v[32:35], v[174:177], v[190:193], v[32:35]
	v_mfma_i32_16x16x64_i8 v[20:23], v[166:169], v[198:201], v[20:23]
	v_mfma_i32_16x16x64_i8 v[16:19], v[174:177], v[198:201], v[16:19]
	v_mfma_i32_16x16x64_i8 v[4:7], v[166:169], v[206:209], v[4:7]
	v_mfma_i32_16x16x64_i8 v[0:3], v[174:177], v[206:209], v[0:3]
	s_setprio 0
	s_barrier
	s_add_i32 s69, s69, 2
	s_add_u32 s28, s28, 0x100
	s_addc_u32 s29, s29, 0
	s_add_u32 s17, s17, 0x100
	s_addc_u32 s19, s19, 0

.LBB0_1851:
	s_lshl_b32 s17, s26, 7
	s_or_b32 s17, s17, s54
	s_mul_i32 s28, s68, 0xe000
	s_mul_hi_i32 s19, s68, 0xe000
	s_add_u32 s30, s55, s28
	s_addc_u32 s19, s56, s19
	s_lshl_b32 s28, s26, 8
	s_ashr_i32 s29, s28, 31
	s_lshl_b64 s[28:29], s[28:29], 2
	v_mbcnt_lo_u32_b32 v78, -1, 0
	v_mbcnt_hi_u32_b32 v78, -1, v78
	s_add_u32 s26, s30, s28
	v_ashrrev_i32_e32 v76, 1, v78
	s_addc_u32 s19, s19, s29
	s_lshl_b32 s28, s54, 2
	v_and_or_b32 v78, v78, 15, s53
	v_and_b32_e32 v166, -8, v76
	s_add_u32 s28, s26, s28
	v_lshl_add_u32 v158, s24, 8, v78
	s_addc_u32 s29, s19, 0
	v_ashrrev_i32_e32 v167, 31, v166
	v_ashrrev_i32_e32 v159, 31, v158
	v_lshl_add_u64 v[76:77], v[166:167], 2, s[28:29]
	v_lshl_add_u64 v[160:161], v[158:159], 2, s[8:9]
	global_load_dword v168, v[160:161], off
	global_load_dwordx4 v[88:91], v[76:77], off
	global_load_dwordx4 v[84:87], v[76:77], off offset:16
	global_load_dwordx4 v[80:83], v[76:77], off offset:512
	s_nop 0
	global_load_dwordx4 v[76:79], v[76:77], off offset:528
	global_load_dword v194, v[160:161], off offset:64
	global_load_dword v196, v[160:161], off offset:128
	global_load_dword v198, v[160:161], off offset:192
	global_load_dword v200, v[160:161], off offset:512
	global_load_dword v202, v[160:161], off offset:576
	global_load_dword v204, v[160:161], off offset:640
	global_load_dword v206, v[160:161], off offset:704
	v_cvt_f32_i32_e32 v141, v141
	v_cvt_f32_i32_e32 v140, v140
	v_cvt_f32_i32_e32 v137, v137
	v_cvt_f32_i32_e32 v136, v136
	v_cvt_f32_i32_e32 v143, v143
	v_cvt_f32_i32_e32 v142, v142
	v_cvt_f32_i32_e32 v139, v139
	v_cvt_f32_i32_e32 v138, v138
	v_cvt_f32_i32_e32 v133, v133
	v_cvt_f32_i32_e32 v132, v132
	v_cvt_f32_i32_e32 v135, v135
	v_cvt_f32_i32_e32 v134, v134
	v_cvt_f32_i32_e32 v173, v131
	v_cvt_f32_i32_e32 v172, v130
	v_cvt_f32_i32_e32 v171, v129
	v_cvt_f32_i32_e32 v170, v128
	v_mov_b32_e32 v174, 0
	v_mov_b32_e32 v175, 0
	v_mov_b64_e32 v[130:131], s[6:7]
	v_add_u32_e32 v128, s17, v166
	v_mad_i64_i32 v[166:167], s[28:29], v158, s62, v[130:131]
	v_or_b32_e32 v176, 16, v158
	v_ashrrev_i32_e32 v129, 31, v128
	v_ashrrev_i32_e32 v177, 31, v176
	v_cvt_f32_i32_e32 v125, v125
	v_cvt_f32_i32_e32 v124, v124
	v_cvt_f32_i32_e32 v121, v121
	v_cvt_f32_i32_e32 v120, v120
	v_cvt_f32_i32_e32 v127, v127
	v_cvt_f32_i32_e32 v126, v126
	v_cvt_f32_i32_e32 v123, v123
	v_cvt_f32_i32_e32 v122, v122
	v_cvt_f32_i32_e32 v113, v113
	v_cvt_f32_i32_e32 v112, v112
	v_cvt_f32_i32_e32 v115, v115
	v_cvt_f32_i32_e32 v114, v114
	v_cvt_f32_i32_e32 v117, v117
	v_cvt_f32_i32_e32 v116, v116
	v_cvt_f32_i32_e32 v119, v119
	v_cvt_f32_i32_e32 v118, v118
	v_cvt_f32_i32_e32 v109, v109
	v_cvt_f32_i32_e32 v108, v108
	v_cvt_f32_i32_e32 v105, v105
	v_cvt_f32_i32_e32 v104, v104
	v_cvt_f32_i32_e32 v111, v111
	v_cvt_f32_i32_e32 v110, v110
	v_cvt_f32_i32_e32 v107, v107
	v_cvt_f32_i32_e32 v106, v106
	v_cvt_f32_i32_e32 v97, v97
	v_cvt_f32_i32_e32 v96, v96
	v_cvt_f32_i32_e32 v99, v99
	v_cvt_f32_i32_e32 v98, v98
	v_cvt_f32_i32_e32 v101, v101
	v_cvt_f32_i32_e32 v100, v100
	v_cvt_f32_i32_e32 v103, v103
	v_cvt_f32_i32_e32 v102, v102
	v_cvt_f32_i32_e32 v93, v93
	v_cvt_f32_i32_e32 v92, v92
	v_cvt_f32_i32_e32 v73, v73
	v_cvt_f32_i32_e32 v72, v72
	v_cvt_f32_i32_e32 v95, v95
	v_cvt_f32_i32_e32 v94, v94
	v_cvt_f32_i32_e32 v75, v75
	v_cvt_f32_i32_e32 v74, v74
	v_cvt_f32_i32_e32 v65, v65
	v_cvt_f32_i32_e32 v64, v64
	v_cvt_f32_i32_e32 v67, v67
	v_cvt_f32_i32_e32 v66, v66
	v_cvt_f32_i32_e32 v69, v69
	v_cvt_f32_i32_e32 v68, v68
	v_cvt_f32_i32_e32 v71, v71
	v_cvt_f32_i32_e32 v70, v70
	v_cvt_f32_i32_e32 v61, v61
	v_cvt_f32_i32_e32 v60, v60
	v_cvt_f32_i32_e32 v57, v57
	s_and_b64 vcc, exec, s[10:11]
	s_cbranch_vccz .Lalign_p12
	s_barrier
.Lalign_p12:
	s_waitcnt vmcnt(7)
	v_pk_mul_f32 v[180:181], v[88:89], v[168:169] op_sel_hi:[1,0]
	v_pk_mul_f32 v[184:185], v[84:85], v[168:169] op_sel_hi:[1,0]
	v_pk_mul_f32 v[178:179], v[90:91], v[168:169] op_sel_hi:[1,0]
	v_pk_mul_f32 v[182:183], v[86:87], v[168:169] op_sel_hi:[1,0]
	v_pk_mul_f32 v[186:187], v[80:81], v[168:169] op_sel_hi:[1,0]
	v_pk_mul_f32 v[188:189], v[82:83], v[168:169] op_sel_hi:[1,0]
	v_pk_mul_f32 v[140:141], v[180:181], v[140:141]
	v_pk_mul_f32 v[136:137], v[184:185], v[136:137]
	v_pk_mul_f32 v[190:191], v[76:77], v[168:169] op_sel_hi:[1,0]
	v_pk_mul_f32 v[168:169], v[78:79], v[168:169] op_sel_hi:[1,0]
	v_pk_mul_f32 v[142:143], v[178:179], v[142:143]
	v_pk_mul_f32 v[138:139], v[182:183], v[138:139]
	v_pk_mul_f32 v[134:135], v[188:189], v[134:135]
	v_pk_mul_f32 v[132:133], v[186:187], v[132:133]
	v_pk_mul_f32 v[178:179], v[140:141], s[14:15] op_sel_hi:[1,0]
	v_pk_mul_f32 v[182:183], v[136:137], s[14:15] op_sel_hi:[1,0]
	v_pk_mul_f32 v[168:169], v[168:169], v[172:173]
	v_pk_mul_f32 v[172:173], v[142:143], s[14:15] op_sel_hi:[1,0]
	v_pk_mul_f32 v[132:133], v[140:141], v[132:133]
	v_pk_mul_f32 v[134:135], v[142:143], v[134:135]
	v_exp_f32_e32 v140, v178
	v_exp_f32_e32 v142, v182
	v_exp_f32_e32 v141, v179
	v_exp_f32_e32 v143, v183
	v_pk_mul_f32 v[170:171], v[190:191], v[170:171]
	v_pk_mul_f32 v[180:181], v[138:139], s[14:15] op_sel_hi:[1,0]
	v_pk_mul_f32 v[136:137], v[136:137], v[170:171]
	v_pk_mul_f32 v[138:139], v[138:139], v[168:169]
	v_exp_f32_e32 v168, v172
	v_exp_f32_e32 v169, v173
	v_exp_f32_e32 v170, v180
	v_exp_f32_e32 v171, v181
	v_pk_add_f32 v[140:141], v[140:141], 1.0 op_sel_hi:[1,0]
	v_pk_add_f32 v[142:143], v[142:143], 1.0 op_sel_hi:[1,0]
	v_rcp_f32_e32 v140, v140
	v_rcp_f32_e32 v142, v142
	v_rcp_f32_e32 v141, v141
	v_rcp_f32_e32 v143, v143
	v_pk_add_f32 v[168:169], v[168:169], 1.0 op_sel_hi:[1,0]
	v_pk_add_f32 v[170:171], v[170:171], 1.0 op_sel_hi:[1,0]
	v_rcp_f32_e32 v168, v168
	v_rcp_f32_e32 v170, v170
	v_rcp_f32_e32 v169, v169
	v_rcp_f32_e32 v171, v171
	v_pk_mul_f32 v[132:133], v[132:133], v[140:141]
	v_pk_mul_f32 v[136:137], v[136:137], v[142:143]
	v_cvt_pk_fp8_f32 v174, v132, v133
	v_cvt_pk_fp8_f32 v175, v136, v137
	v_pk_mul_f32 v[132:133], v[134:135], v[168:169]
	v_pk_mul_f32 v[134:135], v[138:139], v[170:171]
	v_cvt_pk_fp8_f32 v174, v132, v133 op_sel:[0,0,1]
	v_cvt_pk_fp8_f32 v175, v134, v135 op_sel:[0,0,1]
	v_lshl_add_u64 v[132:133], v[166:167], 0, v[128:129]
	v_or_b32_e32 v136, 32, v158
	global_store_dwordx2 v[132:133], v[174:175], off
	v_mov_b32_e32 v134, 0
	v_mov_b32_e32 v135, 0
	v_mad_i64_i32 v[138:139], s[28:29], v176, s62, v[130:131]
	v_ashrrev_i32_e32 v137, 31, v136
	v_cvt_f32_i32_e32 v56, v56
	v_cvt_f32_i32_e32 v63, v63
	v_cvt_f32_i32_e32 v62, v62
	v_cvt_f32_i32_e32 v59, v59
	v_cvt_f32_i32_e32 v58, v58
	v_cvt_f32_i32_e32 v49, v49
	v_cvt_f32_i32_e32 v48, v48
	v_cvt_f32_i32_e32 v51, v51
	v_cvt_f32_i32_e32 v50, v50
	v_cvt_f32_i32_e32 v53, v53
	v_cvt_f32_i32_e32 v52, v52
	v_cvt_f32_i32_e32 v55, v55
	v_cvt_f32_i32_e32 v54, v54
	v_cvt_f32_i32_e32 v45, v45
	v_cvt_f32_i32_e32 v44, v44
	v_cvt_f32_i32_e32 v41, v41
	v_cvt_f32_i32_e32 v40, v40
	v_cvt_f32_i32_e32 v47, v47
	v_cvt_f32_i32_e32 v46, v46
	v_cvt_f32_i32_e32 v43, v43
	v_cvt_f32_i32_e32 v42, v42
	v_cvt_f32_i32_e32 v33, v33
	v_cvt_f32_i32_e32 v32, v32
	v_cvt_f32_i32_e32 v35, v35
	v_cvt_f32_i32_e32 v34, v34
	v_cvt_f32_i32_e32 v37, v37
	v_cvt_f32_i32_e32 v36, v36
	v_cvt_f32_i32_e32 v39, v39
	v_cvt_f32_i32_e32 v38, v38
	v_cvt_f32_i32_e32 v29, v29
	v_cvt_f32_i32_e32 v28, v28
	v_cvt_f32_i32_e32 v25, v25
	v_cvt_f32_i32_e32 v24, v24
	v_cvt_f32_i32_e32 v31, v31
	v_cvt_f32_i32_e32 v30, v30
	v_cvt_f32_i32_e32 v27, v27
	v_cvt_f32_i32_e32 v26, v26
	v_cvt_f32_i32_e32 v17, v17
	v_cvt_f32_i32_e32 v16, v16
	v_cvt_f32_i32_e32 v19, v19
	v_cvt_f32_i32_e32 v18, v18
	v_cvt_f32_i32_e32 v21, v21
	v_cvt_f32_i32_e32 v20, v20
	v_cvt_f32_i32_e32 v23, v23
	v_cvt_f32_i32_e32 v22, v22
	v_cvt_f32_i32_e32 v13, v13
	v_cvt_f32_i32_e32 v12, v12
	v_cvt_f32_i32_e32 v9, v9
	v_cvt_f32_i32_e32 v8, v8
	v_cvt_f32_i32_e32 v15, v15
	v_cvt_f32_i32_e32 v14, v14
	v_cvt_f32_i32_e32 v11, v11
	v_cvt_f32_i32_e32 v10, v10
	v_cvt_f32_i32_e32 v1, v1
	v_cvt_f32_i32_e32 v0, v0
	v_cvt_f32_i32_e32 v3, v3
	v_cvt_f32_i32_e32 v2, v2
	v_cvt_f32_i32_e32 v5, v5
	v_cvt_f32_i32_e32 v4, v4
	v_cvt_f32_i32_e32 v7, v7
	v_cvt_f32_i32_e32 v6, v6
	s_andn2_b64 vcc, exec, s[0:1]
	s_mov_b64 s[0:1], -1
	s_waitcnt vmcnt(7)
	v_pk_mul_f32 v[142:143], v[88:89], v[194:195] op_sel_hi:[1,0]
	v_pk_mul_f32 v[168:169], v[84:85], v[194:195] op_sel_hi:[1,0]
	v_pk_mul_f32 v[140:141], v[90:91], v[194:195] op_sel_hi:[1,0]
	v_pk_mul_f32 v[166:167], v[86:87], v[194:195] op_sel_hi:[1,0]
	v_pk_mul_f32 v[170:171], v[80:81], v[194:195] op_sel_hi:[1,0]
	v_pk_mul_f32 v[172:173], v[82:83], v[194:195] op_sel_hi:[1,0]
	v_pk_mul_f32 v[174:175], v[76:77], v[194:195] op_sel_hi:[1,0]
	v_pk_mul_f32 v[132:133], v[78:79], v[194:195] op_sel_hi:[1,0]
	v_pk_mul_f32 v[124:125], v[142:143], v[124:125]
	v_pk_mul_f32 v[120:121], v[168:169], v[120:121]
	v_pk_mul_f32 v[126:127], v[140:141], v[126:127]
	v_pk_mul_f32 v[122:123], v[166:167], v[122:123]
	v_pk_mul_f32 v[114:115], v[132:133], v[114:115]
	v_pk_mul_f32 v[112:113], v[174:175], v[112:113]
	v_pk_mul_f32 v[140:141], v[124:125], s[14:15] op_sel_hi:[1,0]
	v_pk_mul_f32 v[166:167], v[120:121], s[14:15] op_sel_hi:[1,0]
	v_pk_mul_f32 v[142:143], v[122:123], s[14:15] op_sel_hi:[1,0]
	v_pk_mul_f32 v[112:113], v[120:121], v[112:113]
	v_pk_mul_f32 v[114:115], v[122:123], v[114:115]
	v_exp_f32_e32 v120, v140
	v_exp_f32_e32 v122, v166
	v_exp_f32_e32 v121, v141
	v_exp_f32_e32 v123, v167
	v_pk_mul_f32 v[118:119], v[172:173], v[118:119]
	v_pk_mul_f32 v[116:117], v[170:171], v[116:117]
	v_pk_mul_f32 v[132:133], v[126:127], s[14:15] op_sel_hi:[1,0]
	v_pk_mul_f32 v[116:117], v[124:125], v[116:117]
	v_pk_mul_f32 v[118:119], v[126:127], v[118:119]
	v_exp_f32_e32 v124, v132
	v_exp_f32_e32 v125, v133
	v_exp_f32_e32 v126, v142
	v_exp_f32_e32 v127, v143
	v_pk_add_f32 v[120:121], v[120:121], 1.0 op_sel_hi:[1,0]
	v_pk_add_f32 v[122:123], v[122:123], 1.0 op_sel_hi:[1,0]
	v_rcp_f32_e32 v120, v120
	v_rcp_f32_e32 v122, v122
	v_rcp_f32_e32 v121, v121
	v_rcp_f32_e32 v123, v123
	v_pk_add_f32 v[124:125], v[124:125], 1.0 op_sel_hi:[1,0]
	v_pk_add_f32 v[126:127], v[126:127], 1.0 op_sel_hi:[1,0]
	v_rcp_f32_e32 v124, v124
	v_rcp_f32_e32 v126, v126
	v_rcp_f32_e32 v125, v125
	v_rcp_f32_e32 v127, v127
	v_pk_mul_f32 v[116:117], v[116:117], v[120:121]
	v_pk_mul_f32 v[112:113], v[112:113], v[122:123]
	v_cvt_pk_fp8_f32 v134, v116, v117
	v_cvt_pk_fp8_f32 v135, v112, v113
	v_pk_mul_f32 v[112:113], v[118:119], v[124:125]
	v_pk_mul_f32 v[114:115], v[114:115], v[126:127]
	v_cvt_pk_fp8_f32 v134, v112, v113 op_sel:[0,0,1]
	v_cvt_pk_fp8_f32 v135, v114, v115 op_sel:[0,0,1]
	v_lshl_add_u64 v[112:113], v[138:139], 0, v[128:129]
	v_mad_i64_i32 v[118:119], s[28:29], v136, s62, v[130:131]
	global_store_dwordx2 v[112:113], v[134:135], off
	v_mov_b32_e32 v114, 0
	v_mov_b32_e32 v115, 0
	v_or_b32_e32 v116, 48, v158
	v_ashrrev_i32_e32 v117, 31, v116
	s_waitcnt vmcnt(7)
	v_pk_mul_f32 v[122:123], v[88:89], v[196:197] op_sel_hi:[1,0]
	v_pk_mul_f32 v[126:127], v[84:85], v[196:197] op_sel_hi:[1,0]
	v_pk_mul_f32 v[120:121], v[90:91], v[196:197] op_sel_hi:[1,0]
	v_pk_mul_f32 v[124:125], v[86:87], v[196:197] op_sel_hi:[1,0]
	v_pk_mul_f32 v[132:133], v[80:81], v[196:197] op_sel_hi:[1,0]
	v_pk_mul_f32 v[134:135], v[82:83], v[196:197] op_sel_hi:[1,0]
	v_pk_mul_f32 v[136:137], v[76:77], v[196:197] op_sel_hi:[1,0]
	v_pk_mul_f32 v[112:113], v[78:79], v[196:197] op_sel_hi:[1,0]
	v_pk_mul_f32 v[108:109], v[122:123], v[108:109]
	v_pk_mul_f32 v[104:105], v[126:127], v[104:105]
	v_pk_mul_f32 v[110:111], v[120:121], v[110:111]
	v_pk_mul_f32 v[106:107], v[124:125], v[106:107]
	v_pk_mul_f32 v[98:99], v[112:113], v[98:99]
	v_pk_mul_f32 v[96:97], v[136:137], v[96:97]
	v_pk_mul_f32 v[120:121], v[108:109], s[14:15] op_sel_hi:[1,0]
	v_pk_mul_f32 v[124:125], v[104:105], s[14:15] op_sel_hi:[1,0]
	v_pk_mul_f32 v[122:123], v[106:107], s[14:15] op_sel_hi:[1,0]
	v_pk_mul_f32 v[96:97], v[104:105], v[96:97]
	v_pk_mul_f32 v[98:99], v[106:107], v[98:99]
	v_exp_f32_e32 v104, v120
	v_exp_f32_e32 v106, v124
	v_exp_f32_e32 v105, v121
	v_exp_f32_e32 v107, v125
	v_pk_mul_f32 v[102:103], v[134:135], v[102:103]
	v_pk_mul_f32 v[100:101], v[132:133], v[100:101]
	v_pk_mul_f32 v[112:113], v[110:111], s[14:15] op_sel_hi:[1,0]
	v_pk_mul_f32 v[100:101], v[108:109], v[100:101]
	v_pk_mul_f32 v[102:103], v[110:111], v[102:103]
	v_exp_f32_e32 v108, v112
	v_exp_f32_e32 v109, v113
	v_exp_f32_e32 v110, v122
	v_exp_f32_e32 v111, v123
	v_pk_add_f32 v[104:105], v[104:105], 1.0 op_sel_hi:[1,0]
	v_pk_add_f32 v[106:107], v[106:107], 1.0 op_sel_hi:[1,0]
	v_rcp_f32_e32 v104, v104
	v_rcp_f32_e32 v106, v106
	v_rcp_f32_e32 v105, v105
	v_rcp_f32_e32 v107, v107
	v_pk_add_f32 v[108:109], v[108:109], 1.0 op_sel_hi:[1,0]
	v_pk_add_f32 v[110:111], v[110:111], 1.0 op_sel_hi:[1,0]
	v_rcp_f32_e32 v108, v108
	v_rcp_f32_e32 v110, v110
	v_rcp_f32_e32 v109, v109
	v_rcp_f32_e32 v111, v111
	v_pk_mul_f32 v[100:101], v[100:101], v[104:105]
	v_pk_mul_f32 v[96:97], v[96:97], v[106:107]
	v_cvt_pk_fp8_f32 v114, v100, v101
	v_cvt_pk_fp8_f32 v115, v96, v97
	v_pk_mul_f32 v[96:97], v[102:103], v[108:109]
	v_pk_mul_f32 v[98:99], v[98:99], v[110:111]
	v_cvt_pk_fp8_f32 v114, v96, v97 op_sel:[0,0,1]
	v_cvt_pk_fp8_f32 v115, v98, v99 op_sel:[0,0,1]
	v_lshl_add_u64 v[96:97], v[118:119], 0, v[128:129]
	global_store_dwordx2 v[96:97], v[114:115], off
	v_mov_b32_e32 v98, 0
	v_mov_b32_e32 v99, 0
	s_waitcnt vmcnt(7)
	v_pk_mul_f32 v[102:103], v[88:89], v[198:199] op_sel_hi:[1,0]
	v_pk_mul_f32 v[106:107], v[84:85], v[198:199] op_sel_hi:[1,0]
	v_pk_mul_f32 v[100:101], v[90:91], v[198:199] op_sel_hi:[1,0]
	v_pk_mul_f32 v[104:105], v[86:87], v[198:199] op_sel_hi:[1,0]
	v_pk_mul_f32 v[108:109], v[80:81], v[198:199] op_sel_hi:[1,0]
	v_pk_mul_f32 v[110:111], v[82:83], v[198:199] op_sel_hi:[1,0]
	v_pk_mul_f32 v[112:113], v[76:77], v[198:199] op_sel_hi:[1,0]
	v_pk_mul_f32 v[96:97], v[78:79], v[198:199] op_sel_hi:[1,0]
	v_pk_mul_f32 v[92:93], v[102:103], v[92:93]
	v_pk_mul_f32 v[72:73], v[106:107], v[72:73]
	v_pk_mul_f32 v[94:95], v[100:101], v[94:95]
	v_pk_mul_f32 v[74:75], v[104:105], v[74:75]
	v_pk_mul_f32 v[66:67], v[96:97], v[66:67]
	v_pk_mul_f32 v[64:65], v[112:113], v[64:65]
	v_pk_mul_f32 v[100:101], v[92:93], s[14:15] op_sel_hi:[1,0]
	v_pk_mul_f32 v[104:105], v[72:73], s[14:15] op_sel_hi:[1,0]
	v_pk_mul_f32 v[102:103], v[74:75], s[14:15] op_sel_hi:[1,0]
	v_pk_mul_f32 v[64:65], v[72:73], v[64:65]
	v_pk_mul_f32 v[66:67], v[74:75], v[66:67]
	v_exp_f32_e32 v72, v100
	v_exp_f32_e32 v74, v104
	v_exp_f32_e32 v73, v101
	v_exp_f32_e32 v75, v105
	v_pk_mul_f32 v[70:71], v[110:111], v[70:71]
	v_pk_mul_f32 v[68:69], v[108:109], v[68:69]
	v_pk_mul_f32 v[96:97], v[94:95], s[14:15] op_sel_hi:[1,0]
	v_pk_mul_f32 v[68:69], v[92:93], v[68:69]
	v_pk_mul_f32 v[70:71], v[94:95], v[70:71]
	v_exp_f32_e32 v92, v96
	v_exp_f32_e32 v93, v97
	v_exp_f32_e32 v94, v102
	v_exp_f32_e32 v95, v103
	v_pk_add_f32 v[72:73], v[72:73], 1.0 op_sel_hi:[1,0]
	v_pk_add_f32 v[74:75], v[74:75], 1.0 op_sel_hi:[1,0]
	v_rcp_f32_e32 v72, v72
	v_rcp_f32_e32 v74, v74
	v_rcp_f32_e32 v73, v73
	v_rcp_f32_e32 v75, v75
	v_pk_add_f32 v[92:93], v[92:93], 1.0 op_sel_hi:[1,0]
	v_pk_add_f32 v[94:95], v[94:95], 1.0 op_sel_hi:[1,0]
	v_rcp_f32_e32 v92, v92
	v_rcp_f32_e32 v94, v94
	v_rcp_f32_e32 v93, v93
	v_rcp_f32_e32 v95, v95
	v_pk_mul_f32 v[68:69], v[68:69], v[72:73]
	v_pk_mul_f32 v[64:65], v[64:65], v[74:75]
	v_cvt_pk_fp8_f32 v98, v68, v69
	v_cvt_pk_fp8_f32 v99, v64, v65
	v_pk_mul_f32 v[64:65], v[70:71], v[92:93]
	v_pk_mul_f32 v[66:67], v[66:67], v[94:95]
	v_cvt_pk_fp8_f32 v98, v64, v65 op_sel:[0,0,1]
	v_cvt_pk_fp8_f32 v99, v66, v67 op_sel:[0,0,1]
	v_mad_i64_i32 v[64:65], s[28:29], v116, s62, v[130:131]
	v_lshl_add_u64 v[64:65], v[64:65], 0, v[128:129]
	global_store_dwordx2 v[64:65], v[98:99], off
	v_mov_b32_e32 v66, 0
	v_mov_b32_e32 v67, 0
	v_add_u32_e32 v98, 0x80, v158
	s_waitcnt vmcnt(7)
	v_pk_mul_f32 v[70:71], v[88:89], v[200:201] op_sel_hi:[1,0]
	v_pk_mul_f32 v[74:75], v[84:85], v[200:201] op_sel_hi:[1,0]
	v_pk_mul_f32 v[68:69], v[90:91], v[200:201] op_sel_hi:[1,0]
	v_pk_mul_f32 v[72:73], v[86:87], v[200:201] op_sel_hi:[1,0]
	v_pk_mul_f32 v[92:93], v[80:81], v[200:201] op_sel_hi:[1,0]
	v_pk_mul_f32 v[94:95], v[82:83], v[200:201] op_sel_hi:[1,0]
	v_pk_mul_f32 v[96:97], v[76:77], v[200:201] op_sel_hi:[1,0]
	v_pk_mul_f32 v[64:65], v[78:79], v[200:201] op_sel_hi:[1,0]
	v_pk_mul_f32 v[60:61], v[70:71], v[60:61]
	v_pk_mul_f32 v[56:57], v[74:75], v[56:57]
	v_pk_mul_f32 v[62:63], v[68:69], v[62:63]
	v_pk_mul_f32 v[58:59], v[72:73], v[58:59]
	v_pk_mul_f32 v[50:51], v[64:65], v[50:51]
	v_pk_mul_f32 v[48:49], v[96:97], v[48:49]
	v_pk_mul_f32 v[68:69], v[60:61], s[14:15] op_sel_hi:[1,0]
	v_pk_mul_f32 v[72:73], v[56:57], s[14:15] op_sel_hi:[1,0]
	v_pk_mul_f32 v[70:71], v[58:59], s[14:15] op_sel_hi:[1,0]
	v_pk_mul_f32 v[48:49], v[56:57], v[48:49]
	v_pk_mul_f32 v[50:51], v[58:59], v[50:51]
	v_exp_f32_e32 v56, v68
	v_exp_f32_e32 v58, v72
	v_exp_f32_e32 v57, v69
	v_exp_f32_e32 v59, v73
	v_pk_mul_f32 v[54:55], v[94:95], v[54:55]
	v_pk_mul_f32 v[52:53], v[92:93], v[52:53]
	v_pk_mul_f32 v[64:65], v[62:63], s[14:15] op_sel_hi:[1,0]
	v_pk_mul_f32 v[52:53], v[60:61], v[52:53]
	v_pk_mul_f32 v[54:55], v[62:63], v[54:55]
	v_exp_f32_e32 v60, v64
	v_exp_f32_e32 v61, v65
	v_exp_f32_e32 v62, v70
	v_exp_f32_e32 v63, v71
	v_pk_add_f32 v[56:57], v[56:57], 1.0 op_sel_hi:[1,0]
	v_pk_add_f32 v[58:59], v[58:59], 1.0 op_sel_hi:[1,0]
	v_rcp_f32_e32 v56, v56
	v_rcp_f32_e32 v58, v58
	v_rcp_f32_e32 v57, v57
	v_rcp_f32_e32 v59, v59
	v_pk_add_f32 v[60:61], v[60:61], 1.0 op_sel_hi:[1,0]
	v_pk_add_f32 v[62:63], v[62:63], 1.0 op_sel_hi:[1,0]
	v_rcp_f32_e32 v60, v60
	v_rcp_f32_e32 v62, v62
	v_rcp_f32_e32 v61, v61
	v_rcp_f32_e32 v63, v63
	v_pk_mul_f32 v[52:53], v[52:53], v[56:57]
	v_pk_mul_f32 v[48:49], v[48:49], v[58:59]
	v_cvt_pk_fp8_f32 v66, v52, v53
	v_cvt_pk_fp8_f32 v67, v48, v49
	v_pk_mul_f32 v[48:49], v[54:55], v[60:61]
	v_pk_mul_f32 v[50:51], v[50:51], v[62:63]
	v_cvt_pk_fp8_f32 v66, v48, v49 op_sel:[0,0,1]
	v_cvt_pk_fp8_f32 v67, v50, v51 op_sel:[0,0,1]
	v_mad_i64_i32 v[48:49], s[28:29], v98, s62, v[130:131]
	v_lshl_add_u64 v[48:49], v[48:49], 0, v[128:129]
	global_store_dwordx2 v[48:49], v[66:67], off
	v_mov_b32_e32 v50, 0
	v_mov_b32_e32 v51, 0
	v_add_u32_e32 v66, 0x90, v158
	s_waitcnt vmcnt(7)
	v_pk_mul_f32 v[54:55], v[88:89], v[202:203] op_sel_hi:[1,0]
	v_pk_mul_f32 v[58:59], v[84:85], v[202:203] op_sel_hi:[1,0]
	v_pk_mul_f32 v[52:53], v[90:91], v[202:203] op_sel_hi:[1,0]
	v_pk_mul_f32 v[56:57], v[86:87], v[202:203] op_sel_hi:[1,0]
	v_pk_mul_f32 v[60:61], v[80:81], v[202:203] op_sel_hi:[1,0]
	v_pk_mul_f32 v[62:63], v[82:83], v[202:203] op_sel_hi:[1,0]
	v_pk_mul_f32 v[64:65], v[76:77], v[202:203] op_sel_hi:[1,0]
	v_pk_mul_f32 v[48:49], v[78:79], v[202:203] op_sel_hi:[1,0]
	v_pk_mul_f32 v[44:45], v[54:55], v[44:45]
	v_pk_mul_f32 v[40:41], v[58:59], v[40:41]
	v_pk_mul_f32 v[46:47], v[52:53], v[46:47]
	v_pk_mul_f32 v[42:43], v[56:57], v[42:43]
	v_pk_mul_f32 v[34:35], v[48:49], v[34:35]
	v_pk_mul_f32 v[32:33], v[64:65], v[32:33]
	v_pk_mul_f32 v[52:53], v[44:45], s[14:15] op_sel_hi:[1,0]
	v_pk_mul_f32 v[56:57], v[40:41], s[14:15] op_sel_hi:[1,0]
	v_pk_mul_f32 v[54:55], v[42:43], s[14:15] op_sel_hi:[1,0]
	v_pk_mul_f32 v[32:33], v[40:41], v[32:33]
	v_pk_mul_f32 v[34:35], v[42:43], v[34:35]
	v_exp_f32_e32 v40, v52
	v_exp_f32_e32 v42, v56
	v_exp_f32_e32 v41, v53
	v_exp_f32_e32 v43, v57
	v_pk_mul_f32 v[38:39], v[62:63], v[38:39]
	v_pk_mul_f32 v[36:37], v[60:61], v[36:37]
	v_pk_mul_f32 v[48:49], v[46:47], s[14:15] op_sel_hi:[1,0]
	v_pk_mul_f32 v[36:37], v[44:45], v[36:37]
	v_pk_mul_f32 v[38:39], v[46:47], v[38:39]
	v_exp_f32_e32 v44, v48
	v_exp_f32_e32 v45, v49
	v_exp_f32_e32 v46, v54
	v_exp_f32_e32 v47, v55
	v_pk_add_f32 v[40:41], v[40:41], 1.0 op_sel_hi:[1,0]
	v_pk_add_f32 v[42:43], v[42:43], 1.0 op_sel_hi:[1,0]
	v_rcp_f32_e32 v40, v40
	v_rcp_f32_e32 v42, v42
	v_rcp_f32_e32 v41, v41
	v_rcp_f32_e32 v43, v43
	v_pk_add_f32 v[44:45], v[44:45], 1.0 op_sel_hi:[1,0]
	v_pk_add_f32 v[46:47], v[46:47], 1.0 op_sel_hi:[1,0]
	v_rcp_f32_e32 v44, v44
	v_rcp_f32_e32 v46, v46
	v_rcp_f32_e32 v45, v45
	v_rcp_f32_e32 v47, v47
	v_pk_mul_f32 v[36:37], v[36:37], v[40:41]
	v_pk_mul_f32 v[32:33], v[32:33], v[42:43]
	v_cvt_pk_fp8_f32 v50, v36, v37
	v_cvt_pk_fp8_f32 v51, v32, v33
	v_pk_mul_f32 v[32:33], v[38:39], v[44:45]
	v_pk_mul_f32 v[34:35], v[34:35], v[46:47]
	v_cvt_pk_fp8_f32 v50, v32, v33 op_sel:[0,0,1]
	v_cvt_pk_fp8_f32 v51, v34, v35 op_sel:[0,0,1]
	v_mad_i64_i32 v[32:33], s[28:29], v66, s62, v[130:131]
	v_lshl_add_u64 v[32:33], v[32:33], 0, v[128:129]
	global_store_dwordx2 v[32:33], v[50:51], off
	v_mov_b32_e32 v34, 0
	v_mov_b32_e32 v35, 0
	v_add_u32_e32 v50, 0xa0, v158
	s_waitcnt vmcnt(7)
	v_pk_mul_f32 v[38:39], v[88:89], v[204:205] op_sel_hi:[1,0]
	v_pk_mul_f32 v[42:43], v[84:85], v[204:205] op_sel_hi:[1,0]
	v_pk_mul_f32 v[36:37], v[90:91], v[204:205] op_sel_hi:[1,0]
	v_pk_mul_f32 v[40:41], v[86:87], v[204:205] op_sel_hi:[1,0]
	v_pk_mul_f32 v[44:45], v[80:81], v[204:205] op_sel_hi:[1,0]
	v_pk_mul_f32 v[46:47], v[82:83], v[204:205] op_sel_hi:[1,0]
	v_pk_mul_f32 v[48:49], v[76:77], v[204:205] op_sel_hi:[1,0]
	v_pk_mul_f32 v[32:33], v[78:79], v[204:205] op_sel_hi:[1,0]
	v_pk_mul_f32 v[28:29], v[38:39], v[28:29]
	v_pk_mul_f32 v[24:25], v[42:43], v[24:25]
	v_pk_mul_f32 v[30:31], v[36:37], v[30:31]
	v_pk_mul_f32 v[26:27], v[40:41], v[26:27]
	v_pk_mul_f32 v[18:19], v[32:33], v[18:19]
	v_pk_mul_f32 v[16:17], v[48:49], v[16:17]
	v_pk_mul_f32 v[36:37], v[28:29], s[14:15] op_sel_hi:[1,0]
	v_pk_mul_f32 v[40:41], v[24:25], s[14:15] op_sel_hi:[1,0]
	v_pk_mul_f32 v[38:39], v[26:27], s[14:15] op_sel_hi:[1,0]
	v_pk_mul_f32 v[16:17], v[24:25], v[16:17]
	v_pk_mul_f32 v[18:19], v[26:27], v[18:19]
	v_exp_f32_e32 v24, v36
	v_exp_f32_e32 v26, v40
	v_exp_f32_e32 v25, v37
	v_exp_f32_e32 v27, v41
	v_pk_mul_f32 v[22:23], v[46:47], v[22:23]
	v_pk_mul_f32 v[20:21], v[44:45], v[20:21]
	v_pk_mul_f32 v[32:33], v[30:31], s[14:15] op_sel_hi:[1,0]
	v_pk_mul_f32 v[20:21], v[28:29], v[20:21]
	v_pk_mul_f32 v[22:23], v[30:31], v[22:23]
	v_exp_f32_e32 v28, v32
	v_exp_f32_e32 v29, v33
	v_exp_f32_e32 v30, v38
	v_exp_f32_e32 v31, v39
	v_pk_add_f32 v[24:25], v[24:25], 1.0 op_sel_hi:[1,0]
	v_pk_add_f32 v[26:27], v[26:27], 1.0 op_sel_hi:[1,0]
	v_rcp_f32_e32 v24, v24
	v_rcp_f32_e32 v26, v26
	v_rcp_f32_e32 v25, v25
	v_rcp_f32_e32 v27, v27
	v_pk_add_f32 v[28:29], v[28:29], 1.0 op_sel_hi:[1,0]
	v_pk_add_f32 v[30:31], v[30:31], 1.0 op_sel_hi:[1,0]
	v_rcp_f32_e32 v28, v28
	v_rcp_f32_e32 v30, v30
	v_rcp_f32_e32 v29, v29
	v_rcp_f32_e32 v31, v31
	v_pk_mul_f32 v[20:21], v[20:21], v[24:25]
	v_pk_mul_f32 v[16:17], v[16:17], v[26:27]
	v_cvt_pk_fp8_f32 v34, v20, v21
	v_cvt_pk_fp8_f32 v35, v16, v17
	v_pk_mul_f32 v[16:17], v[22:23], v[28:29]
	v_pk_mul_f32 v[18:19], v[18:19], v[30:31]
	v_cvt_pk_fp8_f32 v34, v16, v17 op_sel:[0,0,1]
	v_cvt_pk_fp8_f32 v35, v18, v19 op_sel:[0,0,1]
	v_mad_i64_i32 v[16:17], s[28:29], v50, s62, v[130:131]
	v_lshl_add_u64 v[16:17], v[16:17], 0, v[128:129]
	global_store_dwordx2 v[16:17], v[34:35], off
	v_mov_b32_e32 v18, 0
	v_mov_b32_e32 v19, 0
	v_add_u32_e32 v34, 0xb0, v158
	s_waitcnt vmcnt(7)
	v_pk_mul_f32 v[22:23], v[88:89], v[206:207] op_sel_hi:[1,0]
	v_pk_mul_f32 v[26:27], v[84:85], v[206:207] op_sel_hi:[1,0]
	v_pk_mul_f32 v[20:21], v[90:91], v[206:207] op_sel_hi:[1,0]
	v_pk_mul_f32 v[24:25], v[86:87], v[206:207] op_sel_hi:[1,0]
	v_pk_mul_f32 v[28:29], v[80:81], v[206:207] op_sel_hi:[1,0]
	v_pk_mul_f32 v[30:31], v[82:83], v[206:207] op_sel_hi:[1,0]
	v_pk_mul_f32 v[32:33], v[76:77], v[206:207] op_sel_hi:[1,0]
	v_pk_mul_f32 v[16:17], v[78:79], v[206:207] op_sel_hi:[1,0]
	v_pk_mul_f32 v[12:13], v[22:23], v[12:13]
	v_pk_mul_f32 v[8:9], v[26:27], v[8:9]
	v_pk_mul_f32 v[14:15], v[20:21], v[14:15]
	v_pk_mul_f32 v[10:11], v[24:25], v[10:11]
	v_pk_mul_f32 v[2:3], v[16:17], v[2:3]
	v_pk_mul_f32 v[0:1], v[32:33], v[0:1]
	v_pk_mul_f32 v[20:21], v[12:13], s[14:15] op_sel_hi:[1,0]
	v_pk_mul_f32 v[24:25], v[8:9], s[14:15] op_sel_hi:[1,0]
	v_pk_mul_f32 v[22:23], v[10:11], s[14:15] op_sel_hi:[1,0]
	v_pk_mul_f32 v[0:1], v[8:9], v[0:1]
	v_pk_mul_f32 v[2:3], v[10:11], v[2:3]
	v_exp_f32_e32 v8, v20
	v_exp_f32_e32 v10, v24
	v_exp_f32_e32 v9, v21
	v_exp_f32_e32 v11, v25
	v_pk_mul_f32 v[6:7], v[30:31], v[6:7]
	v_pk_mul_f32 v[4:5], v[28:29], v[4:5]
	v_pk_mul_f32 v[16:17], v[14:15], s[14:15] op_sel_hi:[1,0]
	v_pk_mul_f32 v[4:5], v[12:13], v[4:5]
	v_pk_mul_f32 v[6:7], v[14:15], v[6:7]
	v_exp_f32_e32 v12, v16
	v_exp_f32_e32 v13, v17
	v_exp_f32_e32 v14, v22
	v_exp_f32_e32 v15, v23
	v_pk_add_f32 v[8:9], v[8:9], 1.0 op_sel_hi:[1,0]
	v_pk_add_f32 v[10:11], v[10:11], 1.0 op_sel_hi:[1,0]
	v_rcp_f32_e32 v8, v8
	v_rcp_f32_e32 v10, v10
	v_rcp_f32_e32 v9, v9
	v_rcp_f32_e32 v11, v11
	v_pk_add_f32 v[12:13], v[12:13], 1.0 op_sel_hi:[1,0]
	v_pk_add_f32 v[14:15], v[14:15], 1.0 op_sel_hi:[1,0]
	v_rcp_f32_e32 v12, v12
	v_rcp_f32_e32 v14, v14
	v_rcp_f32_e32 v13, v13
	v_rcp_f32_e32 v15, v15
	v_pk_mul_f32 v[4:5], v[4:5], v[8:9]
	v_pk_mul_f32 v[0:1], v[0:1], v[10:11]
	v_cvt_pk_fp8_f32 v18, v4, v5
	v_cvt_pk_fp8_f32 v19, v0, v1
	v_pk_mul_f32 v[0:1], v[6:7], v[12:13]
	v_pk_mul_f32 v[2:3], v[2:3], v[14:15]
	v_cvt_pk_fp8_f32 v18, v0, v1 op_sel:[0,0,1]
	v_cvt_pk_fp8_f32 v19, v2, v3 op_sel:[0,0,1]
	v_mad_i64_i32 v[0:1], s[28:29], v34, s62, v[130:131]
	v_lshl_add_u64 v[0:1], v[0:1], 0, v[128:129]
	global_store_dwordx2 v[0:1], v[18:19], off
	s_cbranch_vccnz .LBB0_1844
	s_andn2_b64 vcc, exec, s[4:5]
	s_cbranch_vccnz .LBB0_1843
	s_barrier
	s_branch .LBB0_1843
